# baseline (speedup 1.0000x reference)
.LBB2_9:
	s_waitcnt lgkmcnt(0)
	s_nop 1
	v_mfma_f32_32x32x16_bf16 v[80:95], a[192:195], a[128:131], 0
	v_mfma_f32_32x32x16_bf16 v[48:63], a[192:195], a[160:163], 0
	v_mfma_f32_32x32x16_bf16 v[64:79], a[224:227], a[128:131], 0
	v_mfma_f32_32x32x16_bf16 v[32:47], a[224:227], a[160:163], 0
	v_mfma_f32_32x32x16_bf16 v[80:95], a[196:199], a[132:135], v[80:95]
	v_mfma_f32_32x32x16_bf16 v[48:63], a[196:199], a[164:167], v[48:63]
	v_mfma_f32_32x32x16_bf16 v[64:79], a[228:231], a[132:135], v[64:79]
	v_mfma_f32_32x32x16_bf16 v[32:47], a[228:231], a[164:167], v[32:47]
	v_mfma_f32_32x32x16_bf16 v[80:95], a[200:203], a[136:139], v[80:95]
	v_mfma_f32_32x32x16_bf16 v[48:63], a[200:203], a[168:171], v[48:63]
	v_mfma_f32_32x32x16_bf16 v[64:79], a[232:235], a[136:139], v[64:79]
	v_mfma_f32_32x32x16_bf16 v[32:47], a[232:235], a[168:171], v[32:47]
	v_mfma_f32_32x32x16_bf16 v[80:95], a[204:207], a[140:143], v[80:95]
	v_mfma_f32_32x32x16_bf16 v[48:63], a[204:207], a[172:175], v[48:63]
	v_mfma_f32_32x32x16_bf16 v[64:79], a[236:239], a[140:143], v[64:79]
	v_mfma_f32_32x32x16_bf16 v[32:47], a[236:239], a[172:175], v[32:47]
	v_mfma_f32_32x32x16_bf16 v[80:95], a[208:211], a[144:147], v[80:95]
	s_mov_b32 s0, s30
	v_mfma_f32_32x32x16_bf16 v[48:63], a[208:211], a[176:179], v[48:63]
	s_mov_b32 s1, s36
	v_mfma_f32_32x32x16_bf16 v[64:79], a[240:243], a[144:147], v[64:79]
	s_mov_b32 s16, s37
	v_mfma_f32_32x32x16_bf16 v[32:47], a[240:243], a[176:179], v[32:47]
	s_mov_b32 s17, s38
	v_mfma_f32_32x32x16_bf16 v[80:95], a[212:215], a[148:151], v[80:95]
	s_mov_b32 s19, s39
	v_mfma_f32_32x32x16_bf16 v[48:63], a[212:215], a[180:183], v[48:63]
	s_mov_b32 s22, s40
	v_mfma_f32_32x32x16_bf16 v[64:79], a[244:247], a[148:151], v[64:79]
	s_mov_b32 s23, s41
	v_mfma_f32_32x32x16_bf16 v[32:47], a[244:247], a[180:183], v[32:47]
	s_mov_b32 s24, s42
	v_mfma_f32_32x32x16_bf16 v[80:95], a[216:219], a[152:155], v[80:95]
	s_mov_b32 s81, s43
	v_mfma_f32_32x32x16_bf16 v[48:63], a[216:219], a[184:187], v[48:63]
	s_mov_b32 s82, s44
	v_mfma_f32_32x32x16_bf16 v[64:79], a[248:251], a[152:155], v[64:79]
	s_mov_b32 s83, s45
	v_mfma_f32_32x32x16_bf16 v[32:47], a[248:251], a[184:187], v[32:47]
	s_mov_b32 s84, s46
	v_mfma_f32_32x32x16_bf16 v[80:95], a[220:223], a[156:159], v[80:95]
	s_mov_b32 s85, s47
	v_mfma_f32_32x32x16_bf16 v[48:63], a[220:223], a[188:191], v[48:63]
	s_mov_b32 s86, s48
	v_mfma_f32_32x32x16_bf16 v[64:79], a[252:255], a[156:159], v[64:79]
	s_mov_b32 s87, s49
	v_mfma_f32_32x32x16_bf16 v[32:47], a[252:255], a[188:191], v[32:47]
	s_mov_b32 s88, s50
	s_nop 4
	s_waitcnt vmcnt(0) lgkmcnt(0)
	s_barrier
	s_nop 0
	s_mov_b32 m0, s0
	s_nop 0
	buffer_load_dwordx4 v209, s[4:7], s1 offen lds
	s_mov_b32 m0, s16
	ds_read_b128 a[192:195], v219 offset:0
	buffer_load_dwordx4 v210, s[4:7], s17 offen lds
	s_mov_b32 m0, s19
	ds_read_b128 a[196:199], v220 offset:0
	buffer_load_dwordx4 v209, s[4:7], s22 offen lds
	s_mov_b32 m0, s23
	ds_read_b128 a[200:203], v221 offset:0
	buffer_load_dwordx4 v210, s[4:7], s24 offen lds
	s_mov_b32 s22, s6
	s_mov_b32 s23, s7
	s_mov_b32 m0, s81
	ds_read_b128 a[204:207], v222 offset:0
	buffer_load_dwordx4 v211, s[20:23], s82 offen lds
	s_mov_b32 m0, s83
	ds_read_b128 a[208:211], v219 offset:128
	buffer_load_dwordx4 v211, s[20:23], s84 offen lds
	s_mov_b32 m0, s85
	ds_read_b128 a[212:215], v220 offset:128
	buffer_load_dwordx4 v211, s[20:23], s86 offen lds
	s_mov_b32 m0, s87
	ds_read_b128 a[216:219], v221 offset:128
	buffer_load_dwordx4 v211, s[20:23], s88 offen lds
	ds_read_b128 a[220:223], v222 offset:128
	v_max3_f32 v96, v80, v81, v64
	v_max3_f32 v97, v82, v83, v65
	v_max3_f32 v96, v96, v66, v67
	ds_read_b128 a[224:227], v219 offset:8192
	v_max3_f32 v96, v96, v84, v85
	v_max3_f32 v97, v97, v86, v87
	v_max3_f32 v96, v96, v68, v69
	v_max3_f32 v97, v97, v70, v71
	ds_read_b128 a[228:231], v220 offset:8192
	v_max3_f32 v96, v96, v88, v89
	v_max3_f32 v97, v97, v90, v91
	v_max3_f32 v96, v96, v72, v73
	v_max3_f32 v97, v97, v74, v75
	ds_read_b128 a[232:235], v221 offset:8192
	v_max3_f32 v96, v96, v92, v93
	v_max3_f32 v97, v97, v94, v95
	v_max3_f32 v96, v96, v76, v77
	v_max3_f32 v97, v97, v78, v79
	ds_read_b128 a[236:239], v222 offset:8192
	v_max3_f32 v98, v48, v49, v32
	v_max3_f32 v99, v50, v51, v33
	v_max3_f32 v98, v98, v34, v35
	ds_read_b128 a[240:243], v219 offset:8320
	v_max3_f32 v98, v98, v52, v53
	v_max3_f32 v99, v99, v54, v55
	v_max3_f32 v98, v98, v36, v37
	v_max3_f32 v99, v99, v38, v39
	ds_read_b128 a[244:247], v220 offset:8320
	v_max3_f32 v98, v98, v56, v57
	v_max3_f32 v99, v99, v58, v59
	v_max3_f32 v98, v98, v40, v41
	v_max3_f32 v99, v99, v42, v43
	ds_read_b128 a[248:251], v221 offset:8320
	v_max3_f32 v98, v98, v60, v61
	v_max3_f32 v99, v99, v62, v63
	v_max3_f32 v98, v98, v44, v45
	v_max3_f32 v99, v99, v46, v47
	ds_read_b128 a[252:255], v222 offset:8320
	v_max_f32_e32 v96, v96, v97
	v_mov_b32_e32 v97, v96
	s_nop 1
	v_permlane32_swap_b32_e32 v96, v97
	v_max_f32_e32 v227, v96, v97
	v_max_f32_e32 v96, v98, v99
	v_mov_b32_e32 v97, v96
	s_nop 1
	v_permlane32_swap_b32_e32 v96, v97
	v_max_f32_e32 v226, v96, v97
	v_sub_f32_e32 v128, v66, v227
	v_mbcnt_lo_u32_b32 v66, -1, 0
	v_mbcnt_hi_u32_b32 v66, -1, v66
	v_sub_f32_e32 v129, v67, v227
	v_xor_b32_e32 v67, 0x80000000, v227
	v_cmp_gt_u32_e32 vcc, 32, v66
	v_sub_f32_e32 v142, v32, v226
	v_mov_b32_e32 v228, 1.0
	v_sub_f32_e32 v143, v33, v226
	v_xor_b32_e32 v33, 0x80000000, v226
	v_cndmask_b32_e64 v66, 0, 1.0, vcc
	s_nop 1
	v_mfma_f32_32x32x2_f32 v[16:31], v66, v67, 0
	v_mbcnt_lo_u32_b32 v32, -1, 0
	v_mbcnt_hi_u32_b32 v32, -1, v32
	v_sub_f32_e32 v80, v80, v227
	v_sub_f32_e32 v81, v81, v227
	v_sub_f32_e32 v82, v82, v227
	v_sub_f32_e32 v83, v83, v227
	v_sub_f32_e32 v84, v84, v227
	v_sub_f32_e32 v85, v85, v227
	v_sub_f32_e32 v86, v86, v227
	v_sub_f32_e32 v87, v87, v227
	v_sub_f32_e32 v88, v88, v227
	v_sub_f32_e32 v89, v89, v227
	v_sub_f32_e32 v90, v90, v227
	v_sub_f32_e32 v91, v91, v227
	v_sub_f32_e32 v92, v92, v227
	v_sub_f32_e32 v93, v93, v227
	v_sub_f32_e32 v94, v94, v227
	v_sub_f32_e32 v95, v95, v227
	v_sub_f32_e32 v64, v64, v227
	v_sub_f32_e32 v65, v65, v227
	v_sub_f32_e32 v130, v68, v227
	s_nop 0
	v_cmp_gt_u32_e32 vcc, 32, v32
	v_sub_f32_e32 v131, v69, v227
	v_sub_f32_e32 v132, v70, v227
	v_sub_f32_e32 v133, v71, v227
	v_sub_f32_e32 v134, v72, v227
	v_sub_f32_e32 v135, v73, v227
	v_sub_f32_e32 v136, v74, v227
	v_sub_f32_e32 v137, v75, v227
	v_sub_f32_e32 v138, v76, v227
	v_sub_f32_e32 v139, v77, v227
	v_sub_f32_e32 v140, v78, v227
	v_sub_f32_e32 v141, v79, v227
	v_sub_f32_e32 v48, v48, v226
	v_sub_f32_e32 v49, v49, v226
	v_sub_f32_e32 v50, v50, v226
	v_sub_f32_e32 v51, v51, v226
	v_sub_f32_e32 v52, v52, v226
	v_sub_f32_e32 v53, v53, v226
	v_sub_f32_e32 v54, v54, v226
	v_sub_f32_e32 v55, v55, v226
	s_nop 1
	v_cndmask_b32_e64 v32, 0, 1.0, vcc
	v_sub_f32_e32 v56, v56, v226
	v_sub_f32_e32 v57, v57, v226
	v_sub_f32_e32 v58, v58, v226
	v_sub_f32_e32 v59, v59, v226
	v_sub_f32_e32 v60, v60, v226
	v_sub_f32_e32 v61, v61, v226
	v_sub_f32_e32 v62, v62, v226
	v_sub_f32_e32 v63, v63, v226
	v_sub_f32_e32 v144, v34, v226
	v_sub_f32_e32 v145, v35, v226
	v_sub_f32_e32 v146, v36, v226
	v_sub_f32_e32 v147, v37, v226
	v_sub_f32_e32 v183, v38, v226
	v_sub_f32_e32 v192, v39, v226
	v_sub_f32_e32 v193, v40, v226
	v_sub_f32_e32 v194, v41, v226
	v_sub_f32_e32 v195, v42, v226
	v_sub_f32_e32 v196, v43, v226
	v_sub_f32_e32 v197, v44, v226
	v_sub_f32_e32 v199, v45, v226
	v_sub_f32_e32 v229, v46, v226
	v_sub_f32_e32 v231, v47, v226
	s_nop 1
	v_mfma_f32_32x32x2_f32 v[0:15], v32, v33, 0
	v_exp_f32_e32 v112, v80
	v_exp_f32_e32 v113, v81
	v_exp_f32_e32 v114, v82
	v_exp_f32_e32 v115, v83
	v_add_f32_e32 v32, v201, v112
	v_add_f32_e32 v33, v201, v113
	v_exp_f32_e32 v116, v84
	v_exp_f32_e32 v117, v85
	v_exp_f32_e32 v118, v86
	v_add_f32_e32 v32, v32, v114
	v_add_f32_e32 v33, v33, v115
	v_exp_f32_e32 v119, v87
	v_exp_f32_e32 v120, v88
	v_add_f32_e32 v32, v32, v116
	v_add_f32_e32 v33, v33, v117
	v_add_f32_e32 v32, v32, v118
	v_exp_f32_e32 v121, v89
	v_exp_f32_e32 v122, v90
	v_exp_f32_e32 v123, v91
	v_add_f32_e32 v33, v33, v119
	v_add_f32_e32 v32, v32, v120
	v_exp_f32_e32 v124, v92
	v_exp_f32_e32 v125, v93
	v_add_f32_e32 v33, v33, v121
	v_add_f32_e32 v32, v32, v122
	v_add_f32_e32 v33, v33, v123
	v_exp_f32_e32 v126, v94
	v_exp_f32_e32 v127, v95
	v_exp_f32_e32 v96, v48
	v_add_f32_e32 v32, v32, v124
	v_add_f32_e32 v33, v33, v125
	v_exp_f32_e32 v97, v49
	v_exp_f32_e32 v98, v50
	v_add_f32_e32 v232, v32, v126
	v_add_f32_e32 v233, v33, v127
	v_add_f32_e32 v32, v201, v96
	v_exp_f32_e32 v99, v51
	v_exp_f32_e32 v100, v52
	v_exp_f32_e32 v101, v53
	v_add_f32_e32 v33, v201, v97
	v_add_f32_e32 v32, v32, v98
	v_exp_f32_e32 v102, v54
	v_exp_f32_e32 v103, v55
	v_add_f32_e32 v33, v33, v99
	v_add_f32_e32 v32, v32, v100
	v_add_f32_e32 v33, v33, v101
	v_exp_f32_e32 v104, v56
	v_exp_f32_e32 v105, v57
	v_exp_f32_e32 v106, v58
	v_add_f32_e32 v32, v32, v102
	v_add_f32_e32 v33, v33, v103
	v_exp_f32_e32 v107, v59
	v_exp_f32_e32 v108, v60
	v_add_f32_e32 v32, v32, v104
	v_add_f32_e32 v33, v33, v105
	v_add_f32_e32 v32, v32, v106
	v_exp_f32_e32 v109, v61
	v_exp_f32_e32 v110, v62
	v_exp_f32_e32 v111, v63
	v_add_f32_e32 v33, v33, v107
	v_add_f32_e32 v32, v32, v108
	s_nop 0
	s_waitcnt lgkmcnt(0)
	v_add_f32_e32 v33, v33, v109
	v_add_f32_e32 v234, v32, v110
	v_add_f32_e32 v235, v33, v111
	v_mfma_f32_32x32x16_bf16 v[80:95], a[192:195], a[128:131], v[16:31]
	ds_read_b64_tr_b16 v[168:169], v208 offset:0
	v_exp_f32_e32 v236, v64
	v_exp_f32_e32 v237, v65
	v_cvt_pk_bf16_f32 v152, v112, v113
	v_exp_f32_e32 v112, v128
	v_exp_f32_e32 v113, v129
	v_mfma_f32_32x32x16_bf16 v[64:79], a[192:195], a[160:163], v[0:15]
	ds_read_b64_tr_b16 v[170:171], v208 offset:0x800
	v_cvt_pk_bf16_f32 v153, v114, v115
	v_exp_f32_e32 v114, v130
	v_exp_f32_e32 v115, v131
	v_mfma_f32_32x32x16_bf16 v[48:63], a[224:227], a[128:131], v[16:31]
	ds_read_b64_tr_b16 v[172:173], v208 offset:0x200
	v_cvt_pk_bf16_f32 v154, v116, v117
	v_mfma_f32_32x32x16_bf16 v[32:47], a[224:227], a[160:163], v[0:15]
	ds_read_b64_tr_b16 v[174:175], v208 offset:0xa00
	ds_read_b64_tr_b16 v[164:165], v208 offset:0x400
	v_exp_f32_e32 v238, v132
	v_exp_f32_e32 v239, v133
	v_cvt_pk_bf16_f32 v155, v118, v119
	v_exp_f32_e32 v184, v134
	v_exp_f32_e32 v185, v135
	v_mfma_f32_32x32x16_bf16 v[80:95], a[196:199], a[132:135], v[80:95]
	ds_read_b64_tr_b16 v[166:167], v208 offset:0xc00
	v_cvt_pk_bf16_f32 v128, v120, v121
	v_exp_f32_e32 v186, v136
	v_exp_f32_e32 v187, v137
	v_mfma_f32_32x32x16_bf16 v[64:79], a[196:199], a[164:167], v[64:79]
	ds_read_b64_tr_b16 v[176:177], v208 offset:0x600
	v_cvt_pk_bf16_f32 v129, v122, v123
	v_exp_f32_e32 v188, v138
	v_exp_f32_e32 v189, v139
	v_mfma_f32_32x32x16_bf16 v[48:63], a[228:231], a[132:135], v[48:63]
	ds_read_b64_tr_b16 v[178:179], v208 offset:0xe00
	v_cvt_pk_bf16_f32 v130, v124, v125
	v_mfma_f32_32x32x16_bf16 v[32:47], a[228:231], a[164:167], v[32:47]
	ds_read_b64_tr_b16 v[160:161], v208 offset:0x1000
	v_exp_f32_e32 v190, v140
	v_exp_f32_e32 v191, v141
	ds_read_b64_tr_b16 v[162:163], v208 offset:0x1800
	v_cvt_pk_bf16_f32 v131, v126, v127
	v_exp_f32_e32 v141, v142
	v_exp_f32_e32 v142, v143
	v_mfma_f32_32x32x16_bf16 v[80:95], a[200:203], a[136:139], v[80:95]
	ds_read_b64_tr_b16 v[156:157], v208 offset:0x1200
	v_cvt_pk_bf16_f32 v180, v96, v97
	v_exp_f32_e32 v143, v144
	v_mfma_f32_32x32x16_bf16 v[64:79], a[200:203], a[168:171], v[64:79]
	ds_read_b64_tr_b16 v[158:159], v208 offset:0x1a00
	v_exp_f32_e32 v240, v145
	v_cvt_pk_bf16_f32 v181, v98, v99
	v_mfma_f32_32x32x16_bf16 v[48:63], a[232:235], a[136:139], v[48:63]
	ds_read_b64_tr_b16 v[148:149], v208 offset:0x1400
	v_exp_f32_e32 v241, v146
	v_exp_f32_e32 v242, v147
	v_cvt_pk_bf16_f32 v182, v100, v101
	v_mfma_f32_32x32x16_bf16 v[32:47], a[232:235], a[168:171], v[32:47]
	ds_read_b64_tr_b16 v[150:151], v208 offset:0x1c00
	ds_read_b64_tr_b16 v[136:137], v208 offset:0x1600
	v_exp_f32_e32 v243, v183
	v_exp_f32_e32 v244, v192
	v_cvt_pk_bf16_f32 v183, v102, v103
	v_exp_f32_e32 v192, v193
	v_exp_f32_e32 v193, v194
	v_mfma_f32_32x32x16_bf16 v[80:95], a[204:207], a[140:143], v[80:95]
	ds_read_b64_tr_b16 v[138:139], v208 offset:0x1e00
	v_cvt_pk_bf16_f32 v144, v104, v105
	v_exp_f32_e32 v194, v195
	v_exp_f32_e32 v195, v196
	v_mfma_f32_32x32x16_bf16 v[64:79], a[204:207], a[172:175], v[64:79]
	ds_read_b64_tr_b16 v[132:133], v208 offset:0x2000
	v_cvt_pk_bf16_f32 v145, v106, v107
	v_exp_f32_e32 v198, v197
	v_exp_f32_e32 v199, v199
	v_mfma_f32_32x32x16_bf16 v[48:63], a[236:239], a[140:143], v[48:63]
	ds_read_b64_tr_b16 v[134:135], v208 offset:0x2800
	v_cvt_pk_bf16_f32 v146, v108, v109
	v_mfma_f32_32x32x16_bf16 v[32:47], a[236:239], a[172:175], v[32:47]
	ds_read_b64_tr_b16 v[124:125], v208 offset:0x2200
	v_exp_f32_e32 v230, v229
	v_exp_f32_e32 v231, v231
	ds_read_b64_tr_b16 v[126:127], v208 offset:0x2a00
	v_cvt_pk_bf16_f32 v147, v110, v111
	s_mov_b32 s0, s51
	v_mfma_f32_32x32x16_bf16 v[80:95], a[208:211], a[144:147], v[80:95]
	ds_read_b64_tr_b16 v[120:121], v208 offset:0x2400
	v_cvt_pk_bf16_f32 v116, v236, v237
	v_add_f32_e32 v96, v232, v236
	v_add_f32_e32 v97, v233, v237
	s_mov_b32 s1, s52
	v_mfma_f32_32x32x16_bf16 v[64:79], a[208:211], a[176:179], v[64:79]
	ds_read_b64_tr_b16 v[122:123], v208 offset:0x2c00
	v_cvt_pk_bf16_f32 v117, v112, v113
	v_add_f32_e32 v96, v96, v112
	v_add_f32_e32 v97, v97, v113
	s_mov_b32 s16, s53
	v_mfma_f32_32x32x16_bf16 v[48:63], a[240:243], a[144:147], v[48:63]
	ds_read_b64_tr_b16 v[112:113], v208 offset:0x2600
	v_cvt_pk_bf16_f32 v118, v114, v115
	v_add_f32_e32 v96, v96, v114
	v_add_f32_e32 v97, v97, v115
	s_mov_b32 s17, s54
	v_mfma_f32_32x32x16_bf16 v[32:47], a[240:243], a[176:179], v[32:47]
	ds_read_b64_tr_b16 v[114:115], v208 offset:0x2e00
	ds_read_b64_tr_b16 v[108:109], v208 offset:0x3000
	v_cvt_pk_bf16_f32 v119, v238, v239
	v_add_f32_e32 v96, v96, v238
	v_add_f32_e32 v97, v97, v239
	s_mov_b32 s19, s55
	v_mfma_f32_32x32x16_bf16 v[80:95], a[212:215], a[148:151], v[80:95]
	ds_read_b64_tr_b16 v[110:111], v208 offset:0x3800
	v_add_f32_e32 v96, v96, v184
	v_add_f32_e32 v97, v97, v185
	s_mov_b32 s24, s56
	v_mfma_f32_32x32x16_bf16 v[64:79], a[212:215], a[180:183], v[64:79]
	ds_read_b64_tr_b16 v[104:105], v208 offset:0x3200
	v_add_f32_e32 v96, v96, v186
	v_add_f32_e32 v97, v97, v187
	s_mov_b32 s81, s57
	v_mfma_f32_32x32x16_bf16 v[48:63], a[244:247], a[148:151], v[48:63]
	ds_read_b64_tr_b16 v[106:107], v208 offset:0x3a00
	v_add_f32_e32 v96, v96, v188
	v_add_f32_e32 v97, v97, v189
	s_mov_b32 s82, s58
	v_mfma_f32_32x32x16_bf16 v[32:47], a[244:247], a[180:183], v[32:47]
	ds_read_b64_tr_b16 v[100:101], v208 offset:0x3400
	ds_read_b64_tr_b16 v[102:103], v208 offset:0x3c00
	v_add_f32_e32 v196, v96, v190
	v_add_f32_e32 v197, v97, v191
	s_mov_b32 s83, s31
	v_mfma_f32_32x32x16_bf16 v[80:95], a[216:219], a[152:155], v[80:95]
	ds_read_b64_tr_b16 v[96:97], v208 offset:0x3600
	v_cvt_pk_bf16_f32 v140, v141, v142
	v_add_f32_e32 v229, v234, v141
	v_add_f32_e32 v142, v235, v142
	s_mov_b32 s84, s36
	v_mfma_f32_32x32x16_bf16 v[64:79], a[216:219], a[184:187], v[64:79]
	ds_read_b64_tr_b16 v[98:99], v208 offset:0x3e00
	v_cvt_pk_bf16_f32 v141, v143, v240
	v_add_f32_e32 v143, v229, v143
	v_add_f32_e32 v229, v142, v240
	v_mfma_f32_32x32x16_bf16 v[48:63], a[248:251], a[152:155], v[48:63]
	s_mov_b32 s85, s59
	v_cvt_pk_bf16_f32 v142, v241, v242
	v_add_f32_e32 v232, v143, v241
	v_add_f32_e32 v229, v229, v242
	v_mfma_f32_32x32x16_bf16 v[32:47], a[248:251], a[184:187], v[32:47]
	s_mov_b32 s86, s60
	v_cvt_pk_bf16_f32 v143, v243, v244
	v_add_f32_e32 v232, v232, v243
	v_add_f32_e32 v229, v229, v244
	v_mfma_f32_32x32x16_bf16 v[80:95], a[220:223], a[156:159], v[80:95]
	s_mov_b32 s87, s61
	v_add_f32_e32 v232, v232, v192
	v_add_f32_e32 v229, v229, v193
	v_mfma_f32_32x32x16_bf16 v[64:79], a[220:223], a[188:191], v[64:79]
	s_mov_b32 s88, s40
	v_add_f32_e32 v232, v232, v194
	v_add_f32_e32 v229, v229, v195
	v_mfma_f32_32x32x16_bf16 v[48:63], a[252:255], a[156:159], v[48:63]
	s_mov_b32 s89, s62
	v_add_f32_e32 v232, v232, v198
	v_add_f32_e32 v229, v229, v199
	v_mfma_f32_32x32x16_bf16 v[32:47], a[252:255], a[188:191], v[32:47]
	s_mov_b32 s90, s63
	v_add_f32_e32 v232, v232, v230
	v_add_f32_e32 v229, v229, v231
	s_nop 4
	v_add_f32_e32 v196, v196, v197
	s_waitcnt vmcnt(0) lgkmcnt(0)
	s_barrier
	s_nop 0
	v_mov_b32_e32 v197, v196
	s_nop 1
	v_permlane32_swap_b32_e32 v196, v197
	v_add_f32_e32 v196, v196, v197
	v_add_f32_e32 v197, v201, v196
	v_add_f32_e32 v196, v232, v229
	v_mov_b32_e32 v229, v196
	s_nop 1
	v_permlane32_swap_b32_e32 v196, v229
	v_add_f32_e32 v196, v196, v229
	v_add_f32_e32 v196, v201, v196
	s_nop 1
	v_mfma_f32_32x32x16_bf16 a[0:15], v[168:171], v[152:155], 0
	s_mov_b32 m0, s0
	s_nop 0
	buffer_load_dwordx4 v209, s[4:7], s1 offen lds
	v_mfma_f32_32x32x16_bf16 a[16:31], v[168:171], v[180:183], 0
	s_mov_b32 m0, s16
	ds_read_b128 a[192:195], v204 offset:0
	buffer_load_dwordx4 v210, s[4:7], s17 offen lds
	v_mfma_f32_32x32x16_bf16 a[32:47], v[172:175], v[152:155], 0
	s_mov_b32 m0, s19
	ds_read_b128 a[196:199], v205 offset:0
	buffer_load_dwordx4 v209, s[4:7], s24 offen lds
	v_mfma_f32_32x32x16_bf16 a[48:63], v[172:175], v[180:183], 0
	s_mov_b32 m0, s81
	ds_read_b128 a[200:203], v206 offset:0
	buffer_load_dwordx4 v210, s[4:7], s82 offen lds
	v_mfma_f32_32x32x16_bf16 a[64:79], v[164:167], v[152:155], 0
	s_mov_b32 m0, s83
	ds_read_b128 a[204:207], v207 offset:0
	buffer_load_dwordx4 v211, s[20:23], s84 offen lds
	v_mfma_f32_32x32x16_bf16 a[80:95], v[164:167], v[180:183], 0
	s_mov_b32 m0, s85
	ds_read_b128 a[208:211], v204 offset:128
	buffer_load_dwordx4 v211, s[20:23], s86 offen lds
	v_mfma_f32_32x32x16_bf16 a[96:111], v[176:179], v[152:155], 0
	s_mov_b32 m0, s87
	ds_read_b128 a[212:215], v205 offset:128
	buffer_load_dwordx4 v211, s[20:23], s88 offen lds
	v_mfma_f32_32x32x16_bf16 a[112:127], v[176:179], v[180:183], 0
	s_mov_b32 m0, s89
	ds_read_b128 a[216:219], v206 offset:128
	buffer_load_dwordx4 v211, s[20:23], s90 offen lds
	v_mfma_f32_32x32x16_bf16 a[0:15], v[160:163], v[128:131], a[0:15]
	ds_read_b128 a[220:223], v207 offset:128
	v_max3_f32 v152, v80, v81, v48
	v_max3_f32 v153, v82, v83, v49
	v_max3_f32 v152, v152, v50, v51
	v_mfma_f32_32x32x16_bf16 a[16:31], v[160:163], v[144:147], a[16:31]
	ds_read_b128 a[224:227], v204 offset:8192
	v_max3_f32 v152, v152, v84, v85
	v_max3_f32 v153, v153, v86, v87
	v_max3_f32 v152, v152, v52, v53
	v_max3_f32 v153, v153, v54, v55
	v_mfma_f32_32x32x16_bf16 a[32:47], v[156:159], v[128:131], a[32:47]
	ds_read_b128 a[228:231], v205 offset:8192
	v_max3_f32 v152, v152, v88, v89
	v_max3_f32 v153, v153, v90, v91
	v_max3_f32 v152, v152, v56, v57
	v_max3_f32 v153, v153, v58, v59
	v_mfma_f32_32x32x16_bf16 a[48:63], v[156:159], v[144:147], a[48:63]
	ds_read_b128 a[232:235], v206 offset:8192
	v_max3_f32 v152, v152, v92, v93
	v_max3_f32 v153, v153, v94, v95
	v_max3_f32 v152, v152, v60, v61
	v_max3_f32 v153, v153, v62, v63
	v_mfma_f32_32x32x16_bf16 a[64:79], v[148:151], v[128:131], a[64:79]
	ds_read_b128 a[236:239], v207 offset:8192
	v_max3_f32 v154, v64, v65, v32
	v_max3_f32 v155, v66, v67, v33
	v_max3_f32 v154, v154, v34, v35
	v_mfma_f32_32x32x16_bf16 a[80:95], v[148:151], v[144:147], a[80:95]
	ds_read_b128 a[240:243], v204 offset:8320
	v_max3_f32 v148, v154, v68, v69
	v_max3_f32 v149, v155, v70, v71
	v_max3_f32 v148, v148, v36, v37
	v_max3_f32 v149, v149, v38, v39
	v_mfma_f32_32x32x16_bf16 a[96:111], v[136:139], v[128:131], a[96:111]
	ds_read_b128 a[244:247], v205 offset:8320
	v_max3_f32 v128, v148, v72, v73
	v_max3_f32 v129, v149, v74, v75
	v_max3_f32 v128, v128, v40, v41
	v_max3_f32 v129, v129, v42, v43
	v_mfma_f32_32x32x16_bf16 a[112:127], v[136:139], v[144:147], a[112:127]
	ds_read_b128 a[248:251], v206 offset:8320
	v_max3_f32 v128, v128, v76, v77
	v_max3_f32 v129, v129, v78, v79
	v_max3_f32 v128, v128, v44, v45
	v_max3_f32 v130, v129, v46, v47
	v_mfma_f32_32x32x16_bf16 a[0:15], v[132:135], v[116:119], a[0:15]
	ds_read_b128 a[252:255], v207 offset:8320
	v_max_f32_e32 v129, v152, v153
	v_mov_b32_e32 v131, v129
	s_nop 1
	v_permlane32_swap_b32_e32 v129, v131
	v_max_f32_e32 v129, v129, v131
	v_mfma_f32_32x32x16_bf16 a[16:31], v[132:135], v[140:143], a[16:31]
	v_max_f32_e32 v128, v128, v130
	v_mov_b32_e32 v130, v128
	s_nop 1
	v_permlane32_swap_b32_e32 v128, v130
	v_max_f32_e32 v128, v128, v130
	v_max_f32_e32 v130, v129, v129
	v_max_f32_e32 v131, v128, v128
	v_max_f32_e32 v130, v130, v131
	v_mfma_f32_32x32x16_bf16 a[32:47], v[124:127], v[116:119], a[32:47]
	v_cmp_lt_f32_e32 vcc, s79, v130
	s_cmp_lg_u64 vcc, 0
	s_cselect_b64 s[0:1], -1, 0
	s_cbranch_vccnz .LBB2_58
	v_mov_b32_e32 v229, 1.0
.LBB2_11:
	v_cvt_pk_bf16_f32 v156, v184, v185
	v_cvt_pk_bf16_f32 v157, v186, v187
	v_cvt_pk_bf16_f32 v158, v188, v189
	v_cvt_pk_bf16_f32 v159, v190, v191
	v_cvt_pk_bf16_f32 v160, v192, v193
	v_cvt_pk_bf16_f32 v161, v194, v195
	v_cvt_pk_bf16_f32 v162, v198, v199
	v_cvt_pk_bf16_f32 v163, v230, v231
	v_exp_f32_e32 v128, v80
	v_exp_f32_e32 v129, v81
	v_mfma_f32_32x32x16_bf16 a[48:63], v[124:127], v[140:143], a[48:63]
	v_exp_f32_e32 v130, v82
	v_exp_f32_e32 v131, v83
	v_mfma_f32_32x32x16_bf16 a[64:79], v[120:123], v[116:119], a[64:79]
	v_add_f32_e32 v80, v201, v128
	v_add_f32_e32 v81, v201, v129
	v_exp_f32_e32 v132, v84
	v_exp_f32_e32 v133, v85
	v_exp_f32_e32 v134, v86
	v_mfma_f32_32x32x16_bf16 a[80:95], v[120:123], v[140:143], a[80:95]
	v_add_f32_e32 v80, v80, v130
	v_add_f32_e32 v81, v81, v131
	v_exp_f32_e32 v135, v87
	v_exp_f32_e32 v136, v88
	v_mfma_f32_32x32x16_bf16 a[96:111], v[112:115], v[116:119], a[96:111]
	v_add_f32_e32 v80, v80, v132
	v_add_f32_e32 v81, v81, v133
	v_add_f32_e32 v80, v80, v134
	v_exp_f32_e32 v137, v89
	v_exp_f32_e32 v138, v90
	v_exp_f32_e32 v139, v91
	v_mfma_f32_32x32x16_bf16 a[112:127], v[112:115], v[140:143], a[112:127]
	v_add_f32_e32 v81, v81, v135
	v_add_f32_e32 v80, v80, v136
	v_exp_f32_e32 v140, v92
	v_exp_f32_e32 v141, v93
	v_mfma_f32_32x32x16_bf16 a[0:15], v[108:111], v[156:159], a[0:15]
	v_add_f32_e32 v81, v81, v137
	v_add_f32_e32 v80, v80, v138
	v_add_f32_e32 v81, v81, v139
	v_exp_f32_e32 v142, v94
	v_exp_f32_e32 v143, v95
	v_exp_f32_e32 v144, v64
	v_mfma_f32_32x32x16_bf16 a[16:31], v[108:111], v[160:163], a[16:31]
	v_add_f32_e32 v64, v80, v140
	v_add_f32_e32 v80, v81, v141
	v_exp_f32_e32 v145, v65
	v_exp_f32_e32 v146, v66
	v_mfma_f32_32x32x16_bf16 a[32:47], v[104:107], v[156:159], a[32:47]
	v_add_f32_e32 v239, v64, v142
	v_add_f32_e32 v238, v80, v143
	v_add_f32_e32 v64, v201, v144
	v_exp_f32_e32 v147, v67
	v_exp_f32_e32 v148, v68
	v_exp_f32_e32 v149, v69
	v_mfma_f32_32x32x16_bf16 a[48:63], v[104:107], v[160:163], a[48:63]
	v_add_f32_e32 v65, v201, v145
	v_add_f32_e32 v64, v64, v146
	v_exp_f32_e32 v150, v70
	v_exp_f32_e32 v151, v71
	v_mfma_f32_32x32x16_bf16 a[64:79], v[100:103], v[156:159], a[64:79]
	v_add_f32_e32 v65, v65, v147
	v_add_f32_e32 v64, v64, v148
	v_add_f32_e32 v65, v65, v149
	v_exp_f32_e32 v152, v72
	v_exp_f32_e32 v153, v73
	v_exp_f32_e32 v154, v74
	v_mfma_f32_32x32x16_bf16 a[80:95], v[100:103], v[160:163], a[80:95]
	v_add_f32_e32 v64, v64, v150
	v_add_f32_e32 v65, v65, v151
	v_mfma_f32_32x32x16_bf16 a[96:111], v[96:99], v[156:159], a[96:111]
	v_exp_f32_e32 v155, v75
	v_exp_f32_e32 v156, v76
	v_add_f32_e32 v64, v64, v152
	v_add_f32_e32 v65, v65, v153
	v_add_f32_e32 v64, v64, v154
	v_exp_f32_e32 v157, v77
	v_exp_f32_e32 v158, v78
	v_exp_f32_e32 v159, v79
	v_mfma_f32_32x32x16_bf16 a[112:127], v[96:99], v[160:163], a[112:127]
	v_add_f32_e32 v65, v65, v155
	v_add_f32_e32 v64, v64, v156
	s_andn2_b64 vcc, exec, s[0:1]
	v_add_f32_e32 v65, v65, v157
	v_add_f32_e32 v240, v64, v158
	s_nop 0
	v_add_f32_e32 v241, v65, v159
	s_cbranch_vccz .LBB2_59

.LBB2_13:
	v_exp_f32_e32 v48, v48
	v_exp_f32_e32 v49, v49
	v_mfma_f32_32x32x16_bf16 v[112:127], a[192:195], a[128:131], v[16:31]
	ds_read_b64_tr_b16 v[180:181], v223 offset:0
	v_cvt_pk_bf16_f32 v164, v128, v129
	v_exp_f32_e32 v50, v50
	v_exp_f32_e32 v51, v51
	v_mfma_f32_32x32x16_bf16 v[96:111], a[192:195], a[160:163], v[0:15]
	ds_read_b64_tr_b16 v[182:183], v223 offset:0x800
	v_cvt_pk_bf16_f32 v165, v130, v131
	v_mfma_f32_32x32x16_bf16 v[80:95], a[224:227], a[128:131], v[16:31]
	ds_read_b64_tr_b16 v[184:185], v223 offset:0x200
	v_exp_f32_e32 v236, v52
	v_exp_f32_e32 v237, v53
	v_cvt_pk_bf16_f32 v166, v132, v133
	v_mfma_f32_32x32x16_bf16 v[64:79], a[224:227], a[160:163], v[0:15]
	ds_read_b64_tr_b16 v[186:187], v223 offset:0xa00
	ds_read_b64_tr_b16 v[176:177], v223 offset:0x400
	v_exp_f32_e32 v242, v54
	v_exp_f32_e32 v243, v55
	v_cvt_pk_bf16_f32 v167, v134, v135
	v_exp_f32_e32 v198, v56
	v_exp_f32_e32 v199, v57
	v_mfma_f32_32x32x16_bf16 v[112:127], a[196:199], a[132:135], v[112:127]
	ds_read_b64_tr_b16 v[178:179], v223 offset:0xc00
	v_cvt_pk_bf16_f32 v128, v136, v137
	v_exp_f32_e32 v230, v58
	v_exp_f32_e32 v231, v59
	v_mfma_f32_32x32x16_bf16 v[96:111], a[196:199], a[164:167], v[96:111]
	ds_read_b64_tr_b16 v[188:189], v223 offset:0x600
	v_cvt_pk_bf16_f32 v129, v138, v139
	v_exp_f32_e32 v232, v60
	v_exp_f32_e32 v233, v61
	v_mfma_f32_32x32x16_bf16 v[80:95], a[228:231], a[132:135], v[80:95]
	ds_read_b64_tr_b16 v[190:191], v223 offset:0xe00
	v_cvt_pk_bf16_f32 v130, v140, v141
	v_mfma_f32_32x32x16_bf16 v[64:79], a[228:231], a[164:167], v[64:79]
	ds_read_b64_tr_b16 v[172:173], v223 offset:0x1000
	v_exp_f32_e32 v234, v62
	v_exp_f32_e32 v235, v63
	ds_read_b64_tr_b16 v[174:175], v223 offset:0x1800
	v_cvt_pk_bf16_f32 v131, v142, v143
	v_exp_f32_e32 v141, v32
	v_exp_f32_e32 v142, v33
	v_mfma_f32_32x32x16_bf16 v[112:127], a[200:203], a[136:139], v[112:127]
	ds_read_b64_tr_b16 v[168:169], v223 offset:0x1200
	v_cvt_pk_bf16_f32 v192, v144, v145
	v_exp_f32_e32 v143, v34
	v_mfma_f32_32x32x16_bf16 v[96:111], a[200:203], a[168:171], v[96:111]
	ds_read_b64_tr_b16 v[170:171], v223 offset:0x1a00
	v_exp_f32_e32 v244, v35
	v_cvt_pk_bf16_f32 v193, v146, v147
	v_mfma_f32_32x32x16_bf16 v[80:95], a[232:235], a[136:139], v[80:95]
	ds_read_b64_tr_b16 v[160:161], v223 offset:0x1400
	v_exp_f32_e32 v245, v36
	v_exp_f32_e32 v246, v37
	v_cvt_pk_bf16_f32 v194, v148, v149
	v_mfma_f32_32x32x16_bf16 v[64:79], a[232:235], a[168:171], v[64:79]
	ds_read_b64_tr_b16 v[162:163], v223 offset:0x1c00
	ds_read_b64_tr_b16 v[136:137], v223 offset:0x1600
	v_exp_f32_e32 v247, v38
	v_exp_f32_e32 v248, v39
	v_cvt_pk_bf16_f32 v195, v150, v151
	v_exp_f32_e32 v148, v40
	v_exp_f32_e32 v149, v41
	v_mfma_f32_32x32x16_bf16 v[112:127], a[204:207], a[140:143], v[112:127]
	ds_read_b64_tr_b16 v[138:139], v223 offset:0x1e00
	v_cvt_pk_bf16_f32 v144, v152, v153
	v_exp_f32_e32 v150, v42
	v_exp_f32_e32 v151, v43
	v_mfma_f32_32x32x16_bf16 v[96:111], a[204:207], a[172:175], v[96:111]
	ds_read_b64_tr_b16 v[132:133], v223 offset:0x2000
	v_cvt_pk_bf16_f32 v145, v154, v155
	v_exp_f32_e32 v152, v44
	v_exp_f32_e32 v153, v45
	v_mfma_f32_32x32x16_bf16 v[80:95], a[236:239], a[140:143], v[80:95]
	ds_read_b64_tr_b16 v[134:135], v223 offset:0x2800
	v_cvt_pk_bf16_f32 v146, v156, v157
	v_mfma_f32_32x32x16_bf16 v[64:79], a[236:239], a[172:175], v[64:79]
	ds_read_b64_tr_b16 v[60:61], v223 offset:0x2200
	v_exp_f32_e32 v154, v46
	v_exp_f32_e32 v155, v47
	ds_read_b64_tr_b16 v[62:63], v223 offset:0x2a00
	v_cvt_pk_bf16_f32 v147, v158, v159
	s_mov_b32 s0, s30
	v_mfma_f32_32x32x16_bf16 v[112:127], a[208:211], a[144:147], v[112:127]
	ds_read_b64_tr_b16 v[56:57], v223 offset:0x2400
	v_cvt_pk_bf16_f32 v52, v48, v49
	v_add_f32_e32 v32, v239, v48
	v_add_f32_e32 v33, v238, v49
	s_add_i32 s19, s17, 0xfffda000
	s_mov_b32 s1, s19
	v_mfma_f32_32x32x16_bf16 v[96:111], a[208:211], a[176:179], v[96:111]
	ds_read_b64_tr_b16 v[58:59], v223 offset:0x2c00
	v_cvt_pk_bf16_f32 v53, v50, v51
	v_add_f32_e32 v32, v32, v50
	v_add_f32_e32 v33, v33, v51
	s_mov_b32 s81, s37
	v_mfma_f32_32x32x16_bf16 v[80:95], a[240:243], a[144:147], v[80:95]
	ds_read_b64_tr_b16 v[48:49], v223 offset:0x2600
	v_cvt_pk_bf16_f32 v54, v236, v237
	v_add_f32_e32 v32, v32, v236
	v_add_f32_e32 v33, v33, v237
	s_add_i32 s82, s17, 0xfffdc000
	v_mfma_f32_32x32x16_bf16 v[64:79], a[240:243], a[176:179], v[64:79]
	ds_read_b64_tr_b16 v[50:51], v223 offset:0x2e00
	ds_read_b64_tr_b16 v[44:45], v223 offset:0x3000
	v_cvt_pk_bf16_f32 v55, v242, v243
	v_add_f32_e32 v32, v32, v242
	v_add_f32_e32 v33, v33, v243
	s_mov_b32 s83, s39
	v_mfma_f32_32x32x16_bf16 v[112:127], a[212:215], a[148:151], v[112:127]
	ds_read_b64_tr_b16 v[46:47], v223 offset:0x3800
	v_add_f32_e32 v32, v32, v198
	v_add_f32_e32 v33, v33, v199
	s_add_i32 s24, s17, 0xfffde000
	s_mov_b32 s84, s24
	v_mfma_f32_32x32x16_bf16 v[96:111], a[212:215], a[180:183], v[96:111]
	ds_read_b64_tr_b16 v[40:41], v223 offset:0x3200
	v_add_f32_e32 v32, v32, v230
	v_add_f32_e32 v33, v33, v231
	s_mov_b32 s85, s41
	v_mfma_f32_32x32x16_bf16 v[80:95], a[244:247], a[148:151], v[80:95]
	ds_read_b64_tr_b16 v[42:43], v223 offset:0x3a00
	v_add_f32_e32 v32, v32, v232
	v_add_f32_e32 v33, v33, v233
	s_add_i32 s86, s17, 0xfffe0000
	v_mfma_f32_32x32x16_bf16 v[64:79], a[244:247], a[180:183], v[64:79]
	ds_read_b64_tr_b16 v[36:37], v223 offset:0x3400
	ds_read_b64_tr_b16 v[38:39], v223 offset:0x3c00
	v_add_f32_e32 v156, v32, v234
	v_add_f32_e32 v157, v33, v235
	s_mov_b32 s87, s43
	v_mfma_f32_32x32x16_bf16 v[112:127], a[216:219], a[152:155], v[112:127]
	ds_read_b64_tr_b16 v[32:33], v223 offset:0x3600
	v_cvt_pk_bf16_f32 v140, v141, v142
	v_add_f32_e32 v158, v240, v141
	v_add_f32_e32 v142, v241, v142
	s_add_i32 s88, s17, 0xfffba000
	v_mfma_f32_32x32x16_bf16 v[96:111], a[216:219], a[184:187], v[96:111]
	ds_read_b64_tr_b16 v[34:35], v223 offset:0x3e00
	v_cvt_pk_bf16_f32 v141, v143, v244
	v_add_f32_e32 v143, v158, v143
	v_add_f32_e32 v158, v142, v244
	v_mfma_f32_32x32x16_bf16 v[80:95], a[248:251], a[152:155], v[80:95]
	s_mov_b32 s89, s45
	v_cvt_pk_bf16_f32 v142, v245, v246
	v_add_f32_e32 v159, v143, v245
	v_add_f32_e32 v158, v158, v246
	v_mfma_f32_32x32x16_bf16 v[64:79], a[248:251], a[184:187], v[64:79]
	s_add_i32 s90, s17, 0xfffba080
	v_cvt_pk_bf16_f32 v143, v247, v248
	v_add_f32_e32 v159, v159, v247
	v_add_f32_e32 v158, v158, v248
	v_mfma_f32_32x32x16_bf16 v[112:127], a[220:223], a[156:159], v[112:127]
	s_mov_b32 s91, s47
	v_add_f32_e32 v159, v159, v148
	v_add_f32_e32 v158, v158, v149
	v_mfma_f32_32x32x16_bf16 v[96:111], a[220:223], a[188:191], v[96:111]
	s_add_i32 s92, s17, 0xfffbe000
	v_add_f32_e32 v159, v159, v150
	v_add_f32_e32 v158, v158, v151
	v_mfma_f32_32x32x16_bf16 v[80:95], a[252:255], a[156:159], v[80:95]
	s_mov_b32 s93, s49
	v_add_f32_e32 v159, v159, v152
	v_add_f32_e32 v158, v158, v153
	v_mfma_f32_32x32x16_bf16 v[64:79], a[252:255], a[188:191], v[64:79]
	s_add_i32 s94, s17, 0xfffbe080
	v_add_f32_e32 v159, v159, v154
	v_add_f32_e32 v158, v158, v155
	s_nop 4
	v_add_f32_e32 v156, v156, v157
	s_waitcnt vmcnt(0) lgkmcnt(0)
	s_barrier
	s_nop 0
	v_mov_b32_e32 v157, v156
	s_nop 1
	v_permlane32_swap_b32_e32 v156, v157
	v_add_f32_e32 v156, v156, v157
	v_add_f32_e32 v197, v197, v156
	v_add_f32_e32 v156, v159, v158
	v_mov_b32_e32 v157, v156
	s_nop 1
	v_permlane32_swap_b32_e32 v156, v157
	v_add_f32_e32 v156, v156, v157
	v_add_f32_e32 v196, v196, v156
	s_nop 1
	v_mfma_f32_32x32x16_bf16 a[0:15], v[180:183], v[164:167], a[0:15]
	s_mov_b32 m0, s0
	s_nop 0
	buffer_load_dwordx4 v209, s[4:7], s1 offen lds
	v_mfma_f32_32x32x16_bf16 a[16:31], v[180:183], v[192:195], a[16:31]
	s_mov_b32 m0, s81
	ds_read_b128 a[192:195], v219 offset:0
	buffer_load_dwordx4 v210, s[4:7], s82 offen lds
	v_mfma_f32_32x32x16_bf16 a[32:47], v[184:187], v[164:167], a[32:47]
	s_mov_b32 m0, s83
	ds_read_b128 a[196:199], v220 offset:0
	buffer_load_dwordx4 v209, s[4:7], s84 offen lds
	v_mfma_f32_32x32x16_bf16 a[48:63], v[184:187], v[192:195], a[48:63]
	s_mov_b32 m0, s85
	ds_read_b128 a[200:203], v221 offset:0
	buffer_load_dwordx4 v210, s[4:7], s86 offen lds
	v_mfma_f32_32x32x16_bf16 a[64:79], v[176:179], v[164:167], a[64:79]
	s_mov_b32 m0, s87
	ds_read_b128 a[204:207], v222 offset:0
	buffer_load_dwordx4 v211, s[20:23], s88 offen lds
	v_mfma_f32_32x32x16_bf16 a[80:95], v[176:179], v[192:195], a[80:95]
	s_mov_b32 m0, s89
	ds_read_b128 a[208:211], v219 offset:128
	buffer_load_dwordx4 v211, s[20:23], s90 offen lds
	v_mfma_f32_32x32x16_bf16 a[96:111], v[188:191], v[164:167], a[96:111]
	s_mov_b32 m0, s91
	ds_read_b128 a[212:215], v220 offset:128
	buffer_load_dwordx4 v211, s[20:23], s92 offen lds
	v_mfma_f32_32x32x16_bf16 a[112:127], v[188:191], v[192:195], a[112:127]
	s_mov_b32 m0, s93
	ds_read_b128 a[216:219], v221 offset:128
	buffer_load_dwordx4 v211, s[20:23], s94 offen lds
	v_mfma_f32_32x32x16_bf16 a[0:15], v[172:175], v[128:131], a[0:15]
	ds_read_b128 a[220:223], v222 offset:128
	v_max3_f32 v156, v112, v113, v80
	v_max3_f32 v157, v114, v115, v81
	v_max3_f32 v156, v156, v82, v83
	v_mfma_f32_32x32x16_bf16 a[16:31], v[172:175], v[144:147], a[16:31]
	ds_read_b128 a[224:227], v219 offset:8192
	v_max3_f32 v156, v156, v116, v117
	v_max3_f32 v157, v157, v118, v119
	v_max3_f32 v156, v156, v84, v85
	v_max3_f32 v157, v157, v86, v87
	v_mfma_f32_32x32x16_bf16 a[32:47], v[168:171], v[128:131], a[32:47]
	ds_read_b128 a[228:231], v220 offset:8192
	v_max3_f32 v156, v156, v120, v121
	v_max3_f32 v157, v157, v122, v123
	v_max3_f32 v156, v156, v88, v89
	v_max3_f32 v157, v157, v90, v91
	v_mfma_f32_32x32x16_bf16 a[48:63], v[168:171], v[144:147], a[48:63]
	ds_read_b128 a[232:235], v221 offset:8192
	v_max3_f32 v156, v156, v124, v125
	v_max3_f32 v157, v157, v126, v127
	v_max3_f32 v156, v156, v92, v93
	v_max3_f32 v157, v157, v94, v95
	v_mfma_f32_32x32x16_bf16 a[64:79], v[160:163], v[128:131], a[64:79]
	ds_read_b128 a[236:239], v222 offset:8192
	v_max3_f32 v158, v96, v97, v64
	v_max3_f32 v159, v98, v99, v65
	v_max3_f32 v158, v158, v66, v67
	v_mfma_f32_32x32x16_bf16 a[80:95], v[160:163], v[144:147], a[80:95]
	ds_read_b128 a[240:243], v219 offset:8320
	v_max3_f32 v158, v158, v100, v101
	v_max3_f32 v159, v159, v102, v103
	v_max3_f32 v158, v158, v68, v69
	v_max3_f32 v159, v159, v70, v71
	v_mfma_f32_32x32x16_bf16 a[96:111], v[136:139], v[128:131], a[96:111]
	ds_read_b128 a[244:247], v220 offset:8320
	v_max3_f32 v128, v158, v104, v105
	v_max3_f32 v129, v159, v106, v107
	v_max3_f32 v128, v128, v72, v73
	v_max3_f32 v129, v129, v74, v75
	v_mfma_f32_32x32x16_bf16 a[112:127], v[136:139], v[144:147], a[112:127]
	ds_read_b128 a[248:251], v221 offset:8320
	v_max3_f32 v128, v128, v108, v109
	v_max3_f32 v129, v129, v110, v111
	v_max3_f32 v128, v128, v76, v77
	v_max3_f32 v130, v129, v78, v79
	v_mfma_f32_32x32x16_bf16 a[0:15], v[132:135], v[52:55], a[0:15]
	ds_read_b128 a[252:255], v222 offset:8320
	v_max_f32_e32 v129, v156, v157
	v_mov_b32_e32 v131, v129
	s_nop 1
	v_permlane32_swap_b32_e32 v129, v131
	v_max_f32_e32 v129, v129, v131
	v_mfma_f32_32x32x16_bf16 a[16:31], v[132:135], v[140:143], a[16:31]
	v_max_f32_e32 v128, v128, v130
	v_mov_b32_e32 v130, v128
	s_nop 1
	v_permlane32_swap_b32_e32 v128, v130
	v_max_f32_e32 v128, v128, v130
	v_max_f32_e32 v130, v129, v129
	v_max_f32_e32 v131, v128, v128
	v_max_f32_e32 v130, v130, v131
	v_mfma_f32_32x32x16_bf16 a[32:47], v[60:63], v[52:55], a[32:47]
	v_cmp_lt_f32_e32 vcc, s79, v130
	s_cmp_lg_u64 vcc, 0
	s_cselect_b64 s[0:1], -1, 0
	s_cbranch_vccnz .LBB2_18

.LBB2_15:
	s_waitcnt lgkmcnt(0)
	v_exp_f32_e32 v80, v80
	v_exp_f32_e32 v81, v81
	v_mfma_f32_32x32x16_bf16 v[112:127], a[192:195], a[128:131], v[16:31]
	ds_read_b64_tr_b16 v[180:181], v208 offset:0
	v_cvt_pk_bf16_f32 v164, v128, v129
	v_exp_f32_e32 v82, v82
	v_exp_f32_e32 v83, v83
	v_mfma_f32_32x32x16_bf16 v[96:111], a[192:195], a[160:163], v[0:15]
	ds_read_b64_tr_b16 v[182:183], v208 offset:0x800
	v_cvt_pk_bf16_f32 v165, v130, v131
	v_mfma_f32_32x32x16_bf16 v[48:63], a[224:227], a[128:131], v[16:31]
	ds_read_b64_tr_b16 v[184:185], v208 offset:0x200
	v_exp_f32_e32 v240, v84
	v_exp_f32_e32 v241, v85
	v_cvt_pk_bf16_f32 v166, v132, v133
	v_mfma_f32_32x32x16_bf16 v[32:47], a[224:227], a[160:163], v[0:15]
	ds_read_b64_tr_b16 v[186:187], v208 offset:0xa00
	ds_read_b64_tr_b16 v[176:177], v208 offset:0x400
	v_exp_f32_e32 v242, v86
	v_exp_f32_e32 v243, v87
	v_cvt_pk_bf16_f32 v167, v134, v135
	v_exp_f32_e32 v198, v88
	v_exp_f32_e32 v199, v89
	v_mfma_f32_32x32x16_bf16 v[112:127], a[196:199], a[132:135], v[112:127]
	ds_read_b64_tr_b16 v[178:179], v208 offset:0xc00
	v_cvt_pk_bf16_f32 v128, v136, v137
	v_exp_f32_e32 v230, v90
	v_exp_f32_e32 v231, v91
	v_mfma_f32_32x32x16_bf16 v[96:111], a[196:199], a[164:167], v[96:111]
	ds_read_b64_tr_b16 v[188:189], v208 offset:0x600
	v_cvt_pk_bf16_f32 v129, v138, v139
	v_exp_f32_e32 v232, v92
	v_exp_f32_e32 v233, v93
	v_mfma_f32_32x32x16_bf16 v[48:63], a[228:231], a[132:135], v[48:63]
	ds_read_b64_tr_b16 v[190:191], v208 offset:0xe00
	v_cvt_pk_bf16_f32 v130, v140, v141
	v_mfma_f32_32x32x16_bf16 v[32:47], a[228:231], a[164:167], v[32:47]
	ds_read_b64_tr_b16 v[172:173], v208 offset:0x1000
	v_exp_f32_e32 v234, v94
	v_exp_f32_e32 v235, v95
	ds_read_b64_tr_b16 v[174:175], v208 offset:0x1800
	v_cvt_pk_bf16_f32 v131, v142, v143
	v_exp_f32_e32 v141, v64
	v_exp_f32_e32 v142, v65
	v_mfma_f32_32x32x16_bf16 v[112:127], a[200:203], a[136:139], v[112:127]
	ds_read_b64_tr_b16 v[168:169], v208 offset:0x1200
	v_cvt_pk_bf16_f32 v192, v144, v145
	v_exp_f32_e32 v143, v66
	v_mfma_f32_32x32x16_bf16 v[96:111], a[200:203], a[168:171], v[96:111]
	ds_read_b64_tr_b16 v[170:171], v208 offset:0x1a00
	v_exp_f32_e32 v244, v67
	v_cvt_pk_bf16_f32 v193, v146, v147
	v_mfma_f32_32x32x16_bf16 v[48:63], a[232:235], a[136:139], v[48:63]
	ds_read_b64_tr_b16 v[160:161], v208 offset:0x1400
	v_exp_f32_e32 v245, v68
	v_exp_f32_e32 v246, v69
	v_cvt_pk_bf16_f32 v194, v148, v149
	v_mfma_f32_32x32x16_bf16 v[32:47], a[232:235], a[168:171], v[32:47]
	ds_read_b64_tr_b16 v[162:163], v208 offset:0x1c00
	ds_read_b64_tr_b16 v[136:137], v208 offset:0x1600
	v_exp_f32_e32 v247, v70
	v_exp_f32_e32 v248, v71
	v_cvt_pk_bf16_f32 v195, v150, v151
	v_exp_f32_e32 v148, v72
	v_exp_f32_e32 v149, v73
	v_mfma_f32_32x32x16_bf16 v[112:127], a[204:207], a[140:143], v[112:127]
	ds_read_b64_tr_b16 v[138:139], v208 offset:0x1e00
	v_cvt_pk_bf16_f32 v144, v152, v153
	v_exp_f32_e32 v150, v74
	v_exp_f32_e32 v151, v75
	v_mfma_f32_32x32x16_bf16 v[96:111], a[204:207], a[172:175], v[96:111]
	ds_read_b64_tr_b16 v[132:133], v208 offset:0x2000
	v_cvt_pk_bf16_f32 v145, v154, v155
	v_exp_f32_e32 v152, v76
	v_exp_f32_e32 v153, v77
	v_mfma_f32_32x32x16_bf16 v[48:63], a[236:239], a[140:143], v[48:63]
	ds_read_b64_tr_b16 v[134:135], v208 offset:0x2800
	v_cvt_pk_bf16_f32 v146, v156, v157
	v_mfma_f32_32x32x16_bf16 v[32:47], a[236:239], a[172:175], v[32:47]
	ds_read_b64_tr_b16 v[92:93], v208 offset:0x2200
	v_exp_f32_e32 v154, v78
	v_exp_f32_e32 v155, v79
	ds_read_b64_tr_b16 v[94:95], v208 offset:0x2a00
	v_cvt_pk_bf16_f32 v147, v158, v159
	s_mov_b32 s0, s51
	v_mfma_f32_32x32x16_bf16 v[112:127], a[208:211], a[144:147], v[112:127]
	ds_read_b64_tr_b16 v[88:89], v208 offset:0x2400
	v_cvt_pk_bf16_f32 v84, v80, v81
	v_add_f32_e32 v64, v237, v80
	v_add_f32_e32 v65, v236, v81
	s_add_i32 s1, s17, 0xffffa000
	v_mfma_f32_32x32x16_bf16 v[96:111], a[208:211], a[176:179], v[96:111]
	ds_read_b64_tr_b16 v[90:91], v208 offset:0x2c00
	v_cvt_pk_bf16_f32 v85, v82, v83
	v_add_f32_e32 v64, v64, v82
	v_add_f32_e32 v65, v65, v83
	s_mov_b32 s81, s53
	v_mfma_f32_32x32x16_bf16 v[48:63], a[240:243], a[144:147], v[48:63]
	ds_read_b64_tr_b16 v[80:81], v208 offset:0x2600
	v_cvt_pk_bf16_f32 v86, v240, v241
	v_add_f32_e32 v64, v64, v240
	v_add_f32_e32 v65, v65, v241
	s_add_i32 s82, s17, 0xffffc000
	v_mfma_f32_32x32x16_bf16 v[32:47], a[240:243], a[176:179], v[32:47]
	ds_read_b64_tr_b16 v[82:83], v208 offset:0x2e00
	ds_read_b64_tr_b16 v[76:77], v208 offset:0x3000
	v_cvt_pk_bf16_f32 v87, v242, v243
	v_add_f32_e32 v64, v64, v242
	v_add_f32_e32 v65, v65, v243
	s_mov_b32 s83, s55
	v_mfma_f32_32x32x16_bf16 v[112:127], a[212:215], a[148:151], v[112:127]
	ds_read_b64_tr_b16 v[78:79], v208 offset:0x3800
	v_add_f32_e32 v64, v64, v198
	v_add_f32_e32 v65, v65, v199
	s_add_i32 s84, s17, 0xffffe000
	v_mfma_f32_32x32x16_bf16 v[96:111], a[212:215], a[180:183], v[96:111]
	ds_read_b64_tr_b16 v[72:73], v208 offset:0x3200
	v_add_f32_e32 v64, v64, v230
	v_add_f32_e32 v65, v65, v231
	s_mov_b32 s85, s57
	v_mfma_f32_32x32x16_bf16 v[48:63], a[244:247], a[148:151], v[48:63]
	ds_read_b64_tr_b16 v[74:75], v208 offset:0x3a00
	v_add_f32_e32 v64, v64, v232
	v_add_f32_e32 v65, v65, v233
	s_mov_b32 s86, s17
	v_mfma_f32_32x32x16_bf16 v[32:47], a[244:247], a[180:183], v[32:47]
	ds_read_b64_tr_b16 v[68:69], v208 offset:0x3400
	ds_read_b64_tr_b16 v[70:71], v208 offset:0x3c00
	v_add_f32_e32 v156, v64, v234
	v_add_f32_e32 v157, v65, v235
	s_mov_b32 s87, s31
	v_mfma_f32_32x32x16_bf16 v[112:127], a[216:219], a[152:155], v[112:127]
	ds_read_b64_tr_b16 v[64:65], v208 offset:0x3600
	v_cvt_pk_bf16_f32 v140, v141, v142
	v_add_f32_e32 v158, v238, v141
	v_add_f32_e32 v142, v239, v142
	v_mfma_f32_32x32x16_bf16 v[96:111], a[216:219], a[184:187], v[96:111]
	ds_read_b64_tr_b16 v[66:67], v208 offset:0x3e00
	v_cvt_pk_bf16_f32 v141, v143, v244
	v_add_f32_e32 v143, v158, v143
	v_add_f32_e32 v158, v142, v244
	v_mfma_f32_32x32x16_bf16 v[48:63], a[248:251], a[152:155], v[48:63]
	s_mov_b32 s88, s59
	v_cvt_pk_bf16_f32 v142, v245, v246
	v_add_f32_e32 v159, v143, v245
	v_add_f32_e32 v158, v158, v246
	v_mfma_f32_32x32x16_bf16 v[32:47], a[248:251], a[184:187], v[32:47]
	s_add_i32 s89, s17, 0xfffda080
	v_cvt_pk_bf16_f32 v143, v247, v248
	v_add_f32_e32 v159, v159, v247
	v_add_f32_e32 v158, v158, v248
	v_mfma_f32_32x32x16_bf16 v[112:127], a[220:223], a[156:159], v[112:127]
	s_mov_b32 s90, s61
	v_add_f32_e32 v159, v159, v148
	v_add_f32_e32 v158, v158, v149
	v_mfma_f32_32x32x16_bf16 v[96:111], a[220:223], a[188:191], v[96:111]
	v_add_f32_e32 v159, v159, v150
	v_add_f32_e32 v158, v158, v151
	v_mfma_f32_32x32x16_bf16 v[48:63], a[252:255], a[156:159], v[48:63]
	s_mov_b32 s91, s62
	v_add_f32_e32 v159, v159, v152
	v_add_f32_e32 v158, v158, v153
	v_mfma_f32_32x32x16_bf16 v[32:47], a[252:255], a[188:191], v[32:47]
	s_add_i32 s92, s17, 0xfffde080
	v_add_f32_e32 v159, v159, v154
	v_add_f32_e32 v158, v158, v155
	s_nop 4
	v_add_f32_e32 v156, v156, v157
	s_waitcnt vmcnt(0) lgkmcnt(0)
	s_barrier
	s_nop 0
	v_mov_b32_e32 v157, v156
	s_nop 1
	v_permlane32_swap_b32_e32 v156, v157
	v_add_f32_e32 v156, v156, v157
	v_add_f32_e32 v197, v197, v156
	v_add_f32_e32 v156, v159, v158
	v_mov_b32_e32 v157, v156
	s_nop 1
	v_permlane32_swap_b32_e32 v156, v157
	v_add_f32_e32 v156, v156, v157
	v_add_f32_e32 v196, v196, v156
	s_nop 1
	v_mfma_f32_32x32x16_bf16 a[0:15], v[180:183], v[164:167], a[0:15]
	s_mov_b32 m0, s0
	s_nop 0
	buffer_load_dwordx4 v209, s[4:7], s1 offen lds
	v_mfma_f32_32x32x16_bf16 a[16:31], v[180:183], v[192:195], a[16:31]
	s_mov_b32 m0, s81
	ds_read_b128 a[192:195], v204 offset:0
	buffer_load_dwordx4 v210, s[4:7], s82 offen lds
	v_mfma_f32_32x32x16_bf16 a[32:47], v[184:187], v[164:167], a[32:47]
	s_mov_b32 m0, s83
	ds_read_b128 a[196:199], v205 offset:0
	buffer_load_dwordx4 v209, s[4:7], s84 offen lds
	v_mfma_f32_32x32x16_bf16 a[48:63], v[184:187], v[192:195], a[48:63]
	s_mov_b32 m0, s85
	ds_read_b128 a[200:203], v206 offset:0
	buffer_load_dwordx4 v210, s[4:7], s86 offen lds
	v_mfma_f32_32x32x16_bf16 a[64:79], v[176:179], v[164:167], a[64:79]
	s_mov_b32 m0, s87
	ds_read_b128 a[204:207], v207 offset:0
	buffer_load_dwordx4 v211, s[20:23], s19 offen lds
	v_mfma_f32_32x32x16_bf16 a[80:95], v[176:179], v[192:195], a[80:95]
	s_mov_b32 m0, s88
	ds_read_b128 a[208:211], v204 offset:128
	buffer_load_dwordx4 v211, s[20:23], s89 offen lds
	v_mfma_f32_32x32x16_bf16 a[96:111], v[188:191], v[164:167], a[96:111]
	s_mov_b32 m0, s90
	ds_read_b128 a[212:215], v205 offset:128
	buffer_load_dwordx4 v211, s[20:23], s24 offen lds
	v_mfma_f32_32x32x16_bf16 a[112:127], v[188:191], v[192:195], a[112:127]
	s_mov_b32 m0, s91
	ds_read_b128 a[216:219], v206 offset:128
	buffer_load_dwordx4 v211, s[20:23], s92 offen lds
	v_mfma_f32_32x32x16_bf16 a[0:15], v[172:175], v[128:131], a[0:15]
	ds_read_b128 a[220:223], v207 offset:128
	v_max3_f32 v156, v112, v113, v48
	v_max3_f32 v157, v114, v115, v49
	v_max3_f32 v156, v156, v50, v51
	v_mfma_f32_32x32x16_bf16 a[16:31], v[172:175], v[144:147], a[16:31]
	ds_read_b128 a[224:227], v204 offset:8192
	v_max3_f32 v156, v156, v116, v117
	v_max3_f32 v157, v157, v118, v119
	v_max3_f32 v156, v156, v52, v53
	v_max3_f32 v157, v157, v54, v55
	v_mfma_f32_32x32x16_bf16 a[32:47], v[168:171], v[128:131], a[32:47]
	ds_read_b128 a[228:231], v205 offset:8192
	v_max3_f32 v156, v156, v120, v121
	v_max3_f32 v157, v157, v122, v123
	v_max3_f32 v156, v156, v56, v57
	v_max3_f32 v157, v157, v58, v59
	v_mfma_f32_32x32x16_bf16 a[48:63], v[168:171], v[144:147], a[48:63]
	ds_read_b128 a[232:235], v206 offset:8192
	v_max3_f32 v156, v156, v124, v125
	v_max3_f32 v157, v157, v126, v127
	v_max3_f32 v156, v156, v60, v61
	v_max3_f32 v157, v157, v62, v63
	v_mfma_f32_32x32x16_bf16 a[64:79], v[160:163], v[128:131], a[64:79]
	ds_read_b128 a[236:239], v207 offset:8192
	v_max3_f32 v158, v96, v97, v32
	v_max3_f32 v159, v98, v99, v33
	v_max3_f32 v158, v158, v34, v35
	v_mfma_f32_32x32x16_bf16 a[80:95], v[160:163], v[144:147], a[80:95]
	ds_read_b128 a[240:243], v204 offset:8320
	v_max3_f32 v158, v158, v100, v101
	v_max3_f32 v159, v159, v102, v103
	v_max3_f32 v158, v158, v36, v37
	v_max3_f32 v159, v159, v38, v39
	v_mfma_f32_32x32x16_bf16 a[96:111], v[136:139], v[128:131], a[96:111]
	ds_read_b128 a[244:247], v205 offset:8320
	v_max3_f32 v128, v158, v104, v105
	v_max3_f32 v129, v159, v106, v107
	v_max3_f32 v128, v128, v40, v41
	v_max3_f32 v129, v129, v42, v43
	v_mfma_f32_32x32x16_bf16 a[112:127], v[136:139], v[144:147], a[112:127]
	ds_read_b128 a[248:251], v206 offset:8320
	v_max3_f32 v128, v128, v108, v109
	v_max3_f32 v129, v129, v110, v111
	v_max3_f32 v128, v128, v44, v45
	v_max3_f32 v130, v129, v46, v47
	v_mfma_f32_32x32x16_bf16 a[0:15], v[132:135], v[84:87], a[0:15]
	ds_read_b128 a[252:255], v207 offset:8320
	v_max_f32_e32 v129, v156, v157
	v_mov_b32_e32 v131, v129
	s_nop 1
	v_permlane32_swap_b32_e32 v129, v131
	v_max_f32_e32 v129, v129, v131
	v_mfma_f32_32x32x16_bf16 a[16:31], v[132:135], v[140:143], a[16:31]
	v_max_f32_e32 v128, v128, v130
	v_mov_b32_e32 v130, v128
	s_nop 1
	v_permlane32_swap_b32_e32 v128, v130
	v_max_f32_e32 v128, v128, v130
	v_max_f32_e32 v130, v129, v129
	v_max_f32_e32 v131, v128, v128
	v_max_f32_e32 v130, v130, v131
	v_mfma_f32_32x32x16_bf16 a[32:47], v[92:95], v[84:87], a[32:47]
	v_cmp_lt_f32_e32 vcc, s79, v130
	s_cmp_lg_u64 vcc, 0
	s_cselect_b64 s[0:1], -1, 0
	s_cbranch_vccnz .LBB2_20

.LBB2_18:
	v_max_f32_e32 v129, v129, v201
	v_max_f32_e32 v128, v128, v201
	v_exp_f32_e64 v229, -v129
	v_exp_f32_e64 v228, -v128
	v_add_f32_e32 v227, v227, v129
	v_sub_f32_e32 v112, v112, v129
	v_sub_f32_e32 v113, v113, v129
	v_sub_f32_e32 v114, v114, v129
	v_sub_f32_e32 v115, v115, v129
	v_sub_f32_e32 v116, v116, v129
	v_sub_f32_e32 v117, v117, v129
	v_sub_f32_e32 v118, v118, v129
	v_sub_f32_e32 v119, v119, v129
	v_sub_f32_e32 v120, v120, v129
	v_sub_f32_e32 v121, v121, v129
	v_sub_f32_e32 v122, v122, v129
	v_sub_f32_e32 v123, v123, v129
	v_sub_f32_e32 v124, v124, v129
	v_sub_f32_e32 v125, v125, v129
	v_sub_f32_e32 v126, v126, v129
	v_sub_f32_e32 v127, v127, v129
	v_sub_f32_e32 v80, v80, v129
	v_sub_f32_e32 v81, v81, v129
	v_sub_f32_e32 v82, v82, v129
	v_sub_f32_e32 v83, v83, v129
	v_sub_f32_e32 v84, v84, v129
	v_sub_f32_e32 v85, v85, v129
	v_sub_f32_e32 v86, v86, v129
	v_sub_f32_e32 v87, v87, v129
	v_sub_f32_e32 v88, v88, v129
	v_sub_f32_e32 v89, v89, v129
	v_sub_f32_e32 v90, v90, v129
	v_sub_f32_e32 v91, v91, v129
	v_sub_f32_e32 v92, v92, v129
	v_sub_f32_e32 v93, v93, v129
	v_sub_f32_e32 v94, v94, v129
	v_sub_f32_e32 v95, v95, v129
	v_mbcnt_lo_u32_b32 v129, -1, 0
	v_mbcnt_hi_u32_b32 v129, -1, v129
	s_nop 0
	v_xor_b32_e32 v130, 0x80000000, v227
	v_cmp_gt_u32_e32 vcc, 32, v129
	v_add_f32_e32 v226, v226, v128
	v_sub_f32_e32 v96, v96, v128
	v_sub_f32_e32 v97, v97, v128
	v_sub_f32_e32 v98, v98, v128
	v_sub_f32_e32 v99, v99, v128
	v_sub_f32_e32 v100, v100, v128
	v_sub_f32_e32 v101, v101, v128
	v_sub_f32_e32 v102, v102, v128
	v_sub_f32_e32 v103, v103, v128
	v_sub_f32_e32 v104, v104, v128
	v_sub_f32_e32 v105, v105, v128
	v_sub_f32_e32 v106, v106, v128
	v_sub_f32_e32 v107, v107, v128
	v_sub_f32_e32 v108, v108, v128
	v_sub_f32_e32 v109, v109, v128
	v_sub_f32_e32 v110, v110, v128
	v_sub_f32_e32 v111, v111, v128
	v_sub_f32_e32 v64, v64, v128
	v_sub_f32_e32 v65, v65, v128
	s_nop 1
	v_cndmask_b32_e64 v129, 0, 1.0, vcc
	s_nop 1
	v_mfma_f32_32x32x2_f32 v[16:31], v129, v130, 0
	v_sub_f32_e32 v66, v66, v128
	v_sub_f32_e32 v67, v67, v128
	v_sub_f32_e32 v68, v68, v128
	v_sub_f32_e32 v69, v69, v128
	v_sub_f32_e32 v70, v70, v128
	v_sub_f32_e32 v71, v71, v128
	v_sub_f32_e32 v72, v72, v128
	v_sub_f32_e32 v73, v73, v128
	v_sub_f32_e32 v74, v74, v128
	v_sub_f32_e32 v75, v75, v128
	v_sub_f32_e32 v76, v76, v128
	v_sub_f32_e32 v77, v77, v128
	v_sub_f32_e32 v78, v78, v128
	v_sub_f32_e32 v79, v79, v128
	v_mbcnt_lo_u32_b32 v128, -1, 0
	v_mbcnt_hi_u32_b32 v128, -1, v128
	v_xor_b32_e32 v129, 0x80000000, v226
	v_cmp_gt_u32_e32 vcc, 32, v128
	s_nop 1
	v_cndmask_b32_e64 v128, 0, 1.0, vcc
	s_nop 1
	v_mfma_f32_32x32x2_f32 v[0:15], v128, v129, 0
	s_branch .LBB2_14

.LBB2_20:
	v_max_f32_e32 v129, v129, v201
	v_max_f32_e32 v128, v128, v201
	v_exp_f32_e64 v229, -v129
	v_exp_f32_e64 v228, -v128
	v_add_f32_e32 v227, v227, v129
	v_sub_f32_e32 v112, v112, v129
	v_sub_f32_e32 v113, v113, v129
	v_sub_f32_e32 v114, v114, v129
	v_sub_f32_e32 v115, v115, v129
	v_sub_f32_e32 v116, v116, v129
	v_sub_f32_e32 v117, v117, v129
	v_sub_f32_e32 v118, v118, v129
	v_sub_f32_e32 v119, v119, v129
	v_sub_f32_e32 v120, v120, v129
	v_sub_f32_e32 v121, v121, v129
	v_sub_f32_e32 v122, v122, v129
	v_sub_f32_e32 v123, v123, v129
	v_sub_f32_e32 v124, v124, v129
	v_sub_f32_e32 v125, v125, v129
	v_sub_f32_e32 v126, v126, v129
	v_sub_f32_e32 v127, v127, v129
	v_sub_f32_e32 v48, v48, v129
	v_sub_f32_e32 v49, v49, v129
	v_sub_f32_e32 v50, v50, v129
	v_sub_f32_e32 v51, v51, v129
	v_sub_f32_e32 v52, v52, v129
	v_sub_f32_e32 v53, v53, v129
	v_sub_f32_e32 v54, v54, v129
	v_sub_f32_e32 v55, v55, v129
	v_sub_f32_e32 v56, v56, v129
	v_sub_f32_e32 v57, v57, v129
	v_sub_f32_e32 v58, v58, v129
	v_sub_f32_e32 v59, v59, v129
	v_sub_f32_e32 v60, v60, v129
	v_sub_f32_e32 v61, v61, v129
	v_sub_f32_e32 v62, v62, v129
	v_sub_f32_e32 v63, v63, v129
	v_mbcnt_lo_u32_b32 v129, -1, 0
	v_mbcnt_hi_u32_b32 v129, -1, v129
	s_nop 0
	v_xor_b32_e32 v130, 0x80000000, v227
	v_cmp_gt_u32_e32 vcc, 32, v129
	v_add_f32_e32 v226, v226, v128
	v_sub_f32_e32 v96, v96, v128
	v_sub_f32_e32 v97, v97, v128
	v_sub_f32_e32 v98, v98, v128
	v_sub_f32_e32 v99, v99, v128
	v_sub_f32_e32 v100, v100, v128
	v_sub_f32_e32 v101, v101, v128
	v_sub_f32_e32 v102, v102, v128
	v_sub_f32_e32 v103, v103, v128
	v_sub_f32_e32 v104, v104, v128
	v_sub_f32_e32 v105, v105, v128
	v_sub_f32_e32 v106, v106, v128
	v_sub_f32_e32 v107, v107, v128
	v_sub_f32_e32 v108, v108, v128
	v_sub_f32_e32 v109, v109, v128
	v_sub_f32_e32 v110, v110, v128
	v_sub_f32_e32 v111, v111, v128
	v_sub_f32_e32 v32, v32, v128
	v_sub_f32_e32 v33, v33, v128
	s_nop 1
	v_cndmask_b32_e64 v129, 0, 1.0, vcc
	s_nop 1
	v_mfma_f32_32x32x2_f32 v[16:31], v129, v130, 0
	v_sub_f32_e32 v34, v34, v128
	v_sub_f32_e32 v35, v35, v128
	v_sub_f32_e32 v36, v36, v128
	v_sub_f32_e32 v37, v37, v128
	v_sub_f32_e32 v38, v38, v128
	v_sub_f32_e32 v39, v39, v128
	v_sub_f32_e32 v40, v40, v128
	v_sub_f32_e32 v41, v41, v128
	v_sub_f32_e32 v42, v42, v128
	v_sub_f32_e32 v43, v43, v128
	v_sub_f32_e32 v44, v44, v128
	v_sub_f32_e32 v45, v45, v128
	v_sub_f32_e32 v46, v46, v128
	v_sub_f32_e32 v47, v47, v128
	v_mbcnt_lo_u32_b32 v128, -1, 0
	v_mbcnt_hi_u32_b32 v128, -1, v128
	v_xor_b32_e32 v129, 0x80000000, v226
	v_cmp_gt_u32_e32 vcc, 32, v128
	s_nop 1
	v_cndmask_b32_e64 v128, 0, 1.0, vcc
	s_nop 1
	v_mfma_f32_32x32x2_f32 v[0:15], v128, v129, 0
	s_branch .LBB2_16

.LBB2_22:
	v_exp_f32_e32 v48, v48
	v_exp_f32_e32 v49, v49
	v_mfma_f32_32x32x16_bf16 v[112:127], a[192:195], a[128:131], v[16:31]
	ds_read_b64_tr_b16 v[180:181], v223 offset:0
	v_cvt_pk_bf16_f32 v164, v128, v129
	v_exp_f32_e32 v50, v50
	v_exp_f32_e32 v51, v51
	v_mfma_f32_32x32x16_bf16 v[96:111], a[192:195], a[160:163], v[0:15]
	ds_read_b64_tr_b16 v[182:183], v223 offset:0x800
	v_cvt_pk_bf16_f32 v165, v130, v131
	v_exp_f32_e32 v230, v52
	v_exp_f32_e32 v231, v53
	v_mfma_f32_32x32x16_bf16 v[80:95], a[224:227], a[128:131], v[16:31]
	ds_read_b64_tr_b16 v[184:185], v223 offset:0x200
	v_cvt_pk_bf16_f32 v166, v132, v133
	v_mfma_f32_32x32x16_bf16 v[64:79], a[224:227], a[160:163], v[0:15]
	ds_read_b64_tr_b16 v[186:187], v223 offset:0xa00
	ds_read_b64_tr_b16 v[176:177], v223 offset:0x400
	v_exp_f32_e32 v242, v54
	v_exp_f32_e32 v243, v55
	v_cvt_pk_bf16_f32 v167, v134, v135
	v_exp_f32_e32 v198, v56
	v_exp_f32_e32 v199, v57
	v_mfma_f32_32x32x16_bf16 v[112:127], a[196:199], a[132:135], v[112:127]
	ds_read_b64_tr_b16 v[178:179], v223 offset:0xc00
	v_cvt_pk_bf16_f32 v128, v136, v137
	v_exp_f32_e32 v232, v58
	v_exp_f32_e32 v233, v59
	v_mfma_f32_32x32x16_bf16 v[96:111], a[196:199], a[164:167], v[96:111]
	ds_read_b64_tr_b16 v[188:189], v223 offset:0x600
	v_cvt_pk_bf16_f32 v129, v138, v139
	v_exp_f32_e32 v234, v60
	v_exp_f32_e32 v235, v61
	v_mfma_f32_32x32x16_bf16 v[80:95], a[228:231], a[132:135], v[80:95]
	ds_read_b64_tr_b16 v[190:191], v223 offset:0xe00
	v_cvt_pk_bf16_f32 v130, v140, v141
	v_mfma_f32_32x32x16_bf16 v[64:79], a[228:231], a[164:167], v[64:79]
	ds_read_b64_tr_b16 v[172:173], v223 offset:0x1000
	v_exp_f32_e32 v236, v62
	v_exp_f32_e32 v237, v63
	ds_read_b64_tr_b16 v[174:175], v223 offset:0x1800
	v_cvt_pk_bf16_f32 v131, v142, v143
	v_exp_f32_e32 v141, v32
	v_exp_f32_e32 v142, v33
	v_mfma_f32_32x32x16_bf16 v[112:127], a[200:203], a[136:139], v[112:127]
	ds_read_b64_tr_b16 v[168:169], v223 offset:0x1200
	v_cvt_pk_bf16_f32 v192, v144, v145
	v_exp_f32_e32 v143, v34
	v_mfma_f32_32x32x16_bf16 v[96:111], a[200:203], a[168:171], v[96:111]
	ds_read_b64_tr_b16 v[170:171], v223 offset:0x1a00
	v_exp_f32_e32 v244, v35
	v_cvt_pk_bf16_f32 v193, v146, v147
	v_mfma_f32_32x32x16_bf16 v[80:95], a[232:235], a[136:139], v[80:95]
	ds_read_b64_tr_b16 v[160:161], v223 offset:0x1400
	v_exp_f32_e32 v245, v36
	v_exp_f32_e32 v246, v37
	v_cvt_pk_bf16_f32 v194, v148, v149
	v_mfma_f32_32x32x16_bf16 v[64:79], a[232:235], a[168:171], v[64:79]
	ds_read_b64_tr_b16 v[162:163], v223 offset:0x1c00
	ds_read_b64_tr_b16 v[136:137], v223 offset:0x1600
	v_exp_f32_e32 v247, v38
	v_exp_f32_e32 v248, v39
	v_cvt_pk_bf16_f32 v195, v150, v151
	v_exp_f32_e32 v148, v40
	v_exp_f32_e32 v149, v41
	v_mfma_f32_32x32x16_bf16 v[112:127], a[204:207], a[140:143], v[112:127]
	ds_read_b64_tr_b16 v[138:139], v223 offset:0x1e00
	v_cvt_pk_bf16_f32 v144, v152, v153
	v_exp_f32_e32 v150, v42
	v_exp_f32_e32 v151, v43
	v_mfma_f32_32x32x16_bf16 v[96:111], a[204:207], a[172:175], v[96:111]
	ds_read_b64_tr_b16 v[132:133], v223 offset:0x2000
	v_cvt_pk_bf16_f32 v145, v154, v155
	v_exp_f32_e32 v152, v44
	v_exp_f32_e32 v153, v45
	v_mfma_f32_32x32x16_bf16 v[80:95], a[236:239], a[140:143], v[80:95]
	ds_read_b64_tr_b16 v[134:135], v223 offset:0x2800
	v_cvt_pk_bf16_f32 v146, v156, v157
	v_mfma_f32_32x32x16_bf16 v[64:79], a[236:239], a[172:175], v[64:79]
	ds_read_b64_tr_b16 v[60:61], v223 offset:0x2200
	v_exp_f32_e32 v154, v46
	v_exp_f32_e32 v155, v47
	ds_read_b64_tr_b16 v[62:63], v223 offset:0x2a00
	v_cvt_pk_bf16_f32 v147, v158, v159
	s_mov_b32 s0, s30
	v_mfma_f32_32x32x16_bf16 v[112:127], a[208:211], a[144:147], v[112:127]
	ds_read_b64_tr_b16 v[56:57], v223 offset:0x2400
	v_cvt_pk_bf16_f32 v52, v48, v49
	v_add_f32_e32 v32, v239, v48
	v_add_f32_e32 v33, v238, v49
	s_mov_b32 s1, s64
	v_mfma_f32_32x32x16_bf16 v[96:111], a[208:211], a[176:179], v[96:111]
	ds_read_b64_tr_b16 v[58:59], v223 offset:0x2c00
	v_cvt_pk_bf16_f32 v53, v50, v51
	v_add_f32_e32 v32, v32, v50
	v_add_f32_e32 v33, v33, v51
	s_mov_b32 s4, s37
	v_mfma_f32_32x32x16_bf16 v[80:95], a[240:243], a[144:147], v[80:95]
	ds_read_b64_tr_b16 v[48:49], v223 offset:0x2600
	v_cvt_pk_bf16_f32 v54, v230, v231
	v_add_f32_e32 v32, v32, v230
	v_add_f32_e32 v33, v33, v231
	s_mov_b32 s5, s65
	v_mfma_f32_32x32x16_bf16 v[64:79], a[240:243], a[176:179], v[64:79]
	ds_read_b64_tr_b16 v[50:51], v223 offset:0x2e00
	ds_read_b64_tr_b16 v[44:45], v223 offset:0x3000
	v_cvt_pk_bf16_f32 v55, v242, v243
	v_add_f32_e32 v32, v32, v242
	v_add_f32_e32 v33, v33, v243
	s_mov_b32 s16, s39
	v_mfma_f32_32x32x16_bf16 v[112:127], a[212:215], a[148:151], v[112:127]
	ds_read_b64_tr_b16 v[46:47], v223 offset:0x3800
	v_add_f32_e32 v32, v32, v198
	v_add_f32_e32 v33, v33, v199
	s_mov_b32 s17, s66
	v_mfma_f32_32x32x16_bf16 v[96:111], a[212:215], a[180:183], v[96:111]
	ds_read_b64_tr_b16 v[40:41], v223 offset:0x3200
	v_add_f32_e32 v32, v32, v232
	v_add_f32_e32 v33, v33, v233
	s_mov_b32 s19, s41
	v_mfma_f32_32x32x16_bf16 v[80:95], a[244:247], a[148:151], v[80:95]
	ds_read_b64_tr_b16 v[42:43], v223 offset:0x3a00
	v_add_f32_e32 v32, v32, v234
	v_add_f32_e32 v33, v33, v235
	s_mov_b32 s22, s67
	v_mfma_f32_32x32x16_bf16 v[64:79], a[244:247], a[180:183], v[64:79]
	ds_read_b64_tr_b16 v[36:37], v223 offset:0x3400
	ds_read_b64_tr_b16 v[38:39], v223 offset:0x3c00
	v_add_f32_e32 v156, v32, v236
	v_add_f32_e32 v157, v33, v237
	s_mov_b32 s24, s43
	v_mfma_f32_32x32x16_bf16 v[112:127], a[216:219], a[152:155], v[112:127]
	ds_read_b64_tr_b16 v[32:33], v223 offset:0x3600
	v_cvt_pk_bf16_f32 v140, v141, v142
	v_add_f32_e32 v158, v240, v141
	v_add_f32_e32 v142, v241, v142
	s_mov_b32 s81, s68
	v_mfma_f32_32x32x16_bf16 v[96:111], a[216:219], a[184:187], v[96:111]
	ds_read_b64_tr_b16 v[34:35], v223 offset:0x3e00
	v_cvt_pk_bf16_f32 v141, v143, v244
	v_add_f32_e32 v143, v158, v143
	v_add_f32_e32 v158, v142, v244
	v_mfma_f32_32x32x16_bf16 v[80:95], a[248:251], a[152:155], v[80:95]
	s_mov_b32 s82, s45
	v_cvt_pk_bf16_f32 v142, v245, v246
	v_add_f32_e32 v159, v143, v245
	v_add_f32_e32 v158, v158, v246
	v_mfma_f32_32x32x16_bf16 v[64:79], a[248:251], a[184:187], v[64:79]
	s_mov_b32 s83, s69
	v_cvt_pk_bf16_f32 v143, v247, v248
	v_add_f32_e32 v159, v159, v247
	v_add_f32_e32 v158, v158, v248
	v_mfma_f32_32x32x16_bf16 v[112:127], a[220:223], a[156:159], v[112:127]
	s_mov_b32 s84, s47
	v_add_f32_e32 v159, v159, v148
	v_add_f32_e32 v158, v158, v149
	v_mfma_f32_32x32x16_bf16 v[96:111], a[220:223], a[188:191], v[96:111]
	s_mov_b32 s85, s70
	v_add_f32_e32 v159, v159, v150
	v_add_f32_e32 v158, v158, v151
	v_mfma_f32_32x32x16_bf16 v[80:95], a[252:255], a[156:159], v[80:95]
	s_mov_b32 s86, s49
	v_add_f32_e32 v159, v159, v152
	v_add_f32_e32 v158, v158, v153
	v_mfma_f32_32x32x16_bf16 v[64:79], a[252:255], a[188:191], v[64:79]
	s_mov_b32 s87, s71
	v_add_f32_e32 v159, v159, v154
	v_add_f32_e32 v158, v158, v155
	s_nop 4
	v_add_f32_e32 v156, v156, v157
	s_waitcnt vmcnt(0) lgkmcnt(0)
	s_barrier
	s_nop 0
	v_mov_b32_e32 v157, v156
	s_nop 1
	v_permlane32_swap_b32_e32 v156, v157
	v_add_f32_e32 v156, v156, v157
	v_add_f32_e32 v231, v197, v156
	v_add_f32_e32 v156, v159, v158
	v_mov_b32_e32 v157, v156
	s_nop 1
	v_permlane32_swap_b32_e32 v156, v157
	v_add_f32_e32 v156, v156, v157
	v_add_f32_e32 v230, v196, v156
	s_nop 1
	v_mfma_f32_32x32x16_bf16 a[0:15], v[180:183], v[164:167], a[0:15]
	v_mfma_f32_32x32x16_bf16 a[16:31], v[180:183], v[192:195], a[16:31]
	ds_read_b128 a[192:195], v219 offset:0
	v_mfma_f32_32x32x16_bf16 a[32:47], v[184:187], v[164:167], a[32:47]
	ds_read_b128 a[196:199], v220 offset:0
	v_mfma_f32_32x32x16_bf16 a[48:63], v[184:187], v[192:195], a[48:63]
	ds_read_b128 a[200:203], v221 offset:0
	v_mfma_f32_32x32x16_bf16 a[64:79], v[176:179], v[164:167], a[64:79]
	s_mov_b32 s22, s6
	s_mov_b32 s23, s7
	s_mov_b32 m0, s24
	ds_read_b128 a[204:207], v222 offset:0
	buffer_load_dwordx4 v211, s[20:23], s81 offen lds
	v_mfma_f32_32x32x16_bf16 a[80:95], v[176:179], v[192:195], a[80:95]
	s_mov_b32 m0, s82
	ds_read_b128 a[208:211], v219 offset:128
	buffer_load_dwordx4 v211, s[20:23], s83 offen lds
	v_mfma_f32_32x32x16_bf16 a[96:111], v[188:191], v[164:167], a[96:111]
	s_mov_b32 m0, s84
	ds_read_b128 a[212:215], v220 offset:128
	buffer_load_dwordx4 v211, s[20:23], s85 offen lds
	v_mfma_f32_32x32x16_bf16 a[112:127], v[188:191], v[192:195], a[112:127]
	s_mov_b32 m0, s86
	ds_read_b128 a[216:219], v221 offset:128
	buffer_load_dwordx4 v211, s[20:23], s87 offen lds
	v_mfma_f32_32x32x16_bf16 a[0:15], v[172:175], v[128:131], a[0:15]
	ds_read_b128 a[220:223], v222 offset:128
	v_max3_f32 v156, v112, v113, v80
	v_max3_f32 v157, v114, v115, v81
	v_max3_f32 v156, v156, v82, v83
	v_mfma_f32_32x32x16_bf16 a[16:31], v[172:175], v[144:147], a[16:31]
	ds_read_b128 a[224:227], v219 offset:8192
	v_max3_f32 v156, v156, v116, v117
	v_max3_f32 v157, v157, v118, v119
	v_max3_f32 v156, v156, v84, v85
	v_max3_f32 v157, v157, v86, v87
	v_mfma_f32_32x32x16_bf16 a[32:47], v[168:171], v[128:131], a[32:47]
	ds_read_b128 a[228:231], v220 offset:8192
	v_max3_f32 v156, v156, v120, v121
	v_max3_f32 v157, v157, v122, v123
	v_max3_f32 v156, v156, v88, v89
	v_max3_f32 v157, v157, v90, v91
	v_mfma_f32_32x32x16_bf16 a[48:63], v[168:171], v[144:147], a[48:63]
	ds_read_b128 a[232:235], v221 offset:8192
	v_max3_f32 v156, v156, v124, v125
	v_max3_f32 v157, v157, v126, v127
	v_max3_f32 v156, v156, v92, v93
	v_max3_f32 v157, v157, v94, v95
	v_mfma_f32_32x32x16_bf16 a[64:79], v[160:163], v[128:131], a[64:79]
	ds_read_b128 a[236:239], v222 offset:8192
	v_max3_f32 v158, v96, v97, v64
	v_max3_f32 v159, v98, v99, v65
	v_max3_f32 v158, v158, v66, v67
	v_mfma_f32_32x32x16_bf16 a[80:95], v[160:163], v[144:147], a[80:95]
	ds_read_b128 a[240:243], v219 offset:8320
	v_max3_f32 v158, v158, v100, v101
	v_max3_f32 v159, v159, v102, v103
	v_max3_f32 v158, v158, v68, v69
	v_max3_f32 v159, v159, v70, v71
	v_mfma_f32_32x32x16_bf16 a[96:111], v[136:139], v[128:131], a[96:111]
	ds_read_b128 a[244:247], v220 offset:8320
	v_max3_f32 v128, v158, v104, v105
	v_max3_f32 v129, v159, v106, v107
	v_max3_f32 v128, v128, v72, v73
	v_max3_f32 v129, v129, v74, v75
	v_mfma_f32_32x32x16_bf16 a[112:127], v[136:139], v[144:147], a[112:127]
	ds_read_b128 a[248:251], v221 offset:8320
	v_max3_f32 v128, v128, v108, v109
	v_max3_f32 v129, v129, v110, v111
	v_max3_f32 v128, v128, v76, v77
	v_max3_f32 v130, v129, v78, v79
	v_mfma_f32_32x32x16_bf16 a[0:15], v[132:135], v[52:55], a[0:15]
	ds_read_b128 a[252:255], v222 offset:8320
	v_max_f32_e32 v129, v156, v157
	v_mov_b32_e32 v131, v129
	s_nop 1
	v_permlane32_swap_b32_e32 v129, v131
	v_max_f32_e32 v129, v129, v131
	v_mfma_f32_32x32x16_bf16 a[16:31], v[132:135], v[140:143], a[16:31]
	v_max_f32_e32 v128, v128, v130
	v_mov_b32_e32 v130, v128
	s_nop 1
	v_permlane32_swap_b32_e32 v128, v130
	v_max_f32_e32 v128, v128, v130
	v_max_f32_e32 v130, v129, v129
	v_max_f32_e32 v131, v128, v128
	v_max_f32_e32 v130, v130, v131
	v_mfma_f32_32x32x16_bf16 a[32:47], v[60:63], v[52:55], a[32:47]
	v_cmp_lt_f32_e32 vcc, s79, v130
	s_cmp_lg_u64 vcc, 0
	s_cselect_b64 s[0:1], -1, 0
	s_cbranch_vccnz .LBB2_60
.LBB2_23:
	v_cvt_pk_bf16_f32 v156, v198, v199
	v_cvt_pk_bf16_f32 v157, v232, v233
	v_cvt_pk_bf16_f32 v158, v234, v235
	v_cvt_pk_bf16_f32 v159, v236, v237
	v_cvt_pk_bf16_f32 v160, v148, v149
	v_cvt_pk_bf16_f32 v161, v150, v151
	v_cvt_pk_bf16_f32 v162, v152, v153
	v_cvt_pk_bf16_f32 v163, v154, v155
	v_exp_f32_e32 v128, v112
	v_exp_f32_e32 v129, v113
	v_mfma_f32_32x32x16_bf16 a[48:63], v[60:63], v[140:143], a[48:63]
	v_exp_f32_e32 v130, v114
	v_exp_f32_e32 v131, v115
	v_mfma_f32_32x32x16_bf16 a[64:79], v[56:59], v[52:55], a[64:79]
	v_add_f32_e32 v60, v201, v128
	v_add_f32_e32 v61, v201, v129
	v_exp_f32_e32 v132, v116
	v_exp_f32_e32 v133, v117
	v_exp_f32_e32 v134, v118
	v_mfma_f32_32x32x16_bf16 a[80:95], v[56:59], v[140:143], a[80:95]
	v_add_f32_e32 v56, v60, v130
	v_add_f32_e32 v57, v61, v131
	v_exp_f32_e32 v135, v119
	v_exp_f32_e32 v136, v120
	v_mfma_f32_32x32x16_bf16 a[96:111], v[48:51], v[52:55], a[96:111]
	v_add_f32_e32 v52, v56, v132
	v_add_f32_e32 v53, v57, v133
	v_add_f32_e32 v52, v52, v134
	v_exp_f32_e32 v137, v121
	v_exp_f32_e32 v138, v122
	v_exp_f32_e32 v139, v123
	v_mfma_f32_32x32x16_bf16 a[112:127], v[48:51], v[140:143], a[112:127]
	v_add_f32_e32 v48, v53, v135
	v_add_f32_e32 v49, v52, v136
	v_exp_f32_e32 v140, v124
	v_exp_f32_e32 v141, v125
	v_mfma_f32_32x32x16_bf16 a[0:15], v[44:47], v[156:159], a[0:15]
	v_add_f32_e32 v48, v48, v137
	v_add_f32_e32 v49, v49, v138
	v_add_f32_e32 v48, v48, v139
	v_exp_f32_e32 v142, v126
	v_exp_f32_e32 v143, v127
	v_exp_f32_e32 v144, v96
	v_mfma_f32_32x32x16_bf16 a[16:31], v[44:47], v[160:163], a[16:31]
	v_add_f32_e32 v44, v49, v140
	v_add_f32_e32 v45, v48, v141
	v_exp_f32_e32 v145, v97
	v_exp_f32_e32 v146, v98
	v_mfma_f32_32x32x16_bf16 a[32:47], v[40:43], v[156:159], a[32:47]
	v_add_f32_e32 v237, v44, v142
	v_add_f32_e32 v236, v45, v143
	v_add_f32_e32 v44, v201, v144
	v_exp_f32_e32 v147, v99
	v_exp_f32_e32 v148, v100
	v_exp_f32_e32 v149, v101
	v_mfma_f32_32x32x16_bf16 a[48:63], v[40:43], v[160:163], a[48:63]
	v_add_f32_e32 v40, v201, v145
	v_add_f32_e32 v41, v44, v146
	v_exp_f32_e32 v150, v102
	v_exp_f32_e32 v151, v103
	v_mfma_f32_32x32x16_bf16 a[64:79], v[36:39], v[156:159], a[64:79]
	v_add_f32_e32 v40, v40, v147
	v_add_f32_e32 v41, v41, v148
	v_add_f32_e32 v40, v40, v149
	v_exp_f32_e32 v152, v104
	v_exp_f32_e32 v153, v105
	v_exp_f32_e32 v154, v106
	v_mfma_f32_32x32x16_bf16 a[80:95], v[36:39], v[160:163], a[80:95]
	v_add_f32_e32 v36, v41, v150
	v_add_f32_e32 v37, v40, v151
	v_mfma_f32_32x32x16_bf16 a[96:111], v[32:35], v[156:159], a[96:111]
	v_exp_f32_e32 v155, v107
	v_exp_f32_e32 v156, v108
	v_add_f32_e32 v36, v36, v152
	v_add_f32_e32 v37, v37, v153
	v_add_f32_e32 v36, v36, v154
	v_exp_f32_e32 v157, v109
	v_exp_f32_e32 v158, v110
	v_exp_f32_e32 v159, v111
	v_mfma_f32_32x32x16_bf16 a[112:127], v[32:35], v[160:163], a[112:127]
	v_add_f32_e32 v32, v37, v155
	v_add_f32_e32 v33, v36, v156
	s_andn2_b64 vcc, exec, s[0:1]
	v_add_f32_e32 v32, v32, v157
	v_add_f32_e32 v238, v33, v158
	s_nop 0
	v_add_f32_e32 v239, v32, v159
	s_cbranch_vccz .LBB2_61
.LBB2_24:
	s_waitcnt lgkmcnt(0)
	v_mfma_f32_32x32x16_bf16 v[112:127], a[192:195], a[128:131], v[16:31]
	ds_read_b64_tr_b16 v[176:177], v208 offset:0
	v_exp_f32_e32 v240, v80
	v_exp_f32_e32 v241, v81
	v_cvt_pk_bf16_f32 v168, v128, v129
	v_exp_f32_e32 v82, v82
	v_exp_f32_e32 v83, v83
	v_mfma_f32_32x32x16_bf16 v[96:111], a[192:195], a[160:163], v[0:15]
	ds_read_b64_tr_b16 v[178:179], v208 offset:0x800
	v_cvt_pk_bf16_f32 v169, v130, v131
	v_exp_f32_e32 v84, v84
	v_exp_f32_e32 v85, v85
	v_mfma_f32_32x32x16_bf16 v[48:63], a[224:227], a[128:131], v[16:31]
	ds_read_b64_tr_b16 v[180:181], v208 offset:0x200
	v_cvt_pk_bf16_f32 v170, v132, v133
	v_mfma_f32_32x32x16_bf16 v[32:47], a[224:227], a[160:163], v[0:15]
	ds_read_b64_tr_b16 v[182:183], v208 offset:0xa00
	v_exp_f32_e32 v86, v86
	v_exp_f32_e32 v87, v87
	ds_read_b64_tr_b16 v[184:185], v208 offset:0x400
	v_cvt_pk_bf16_f32 v171, v134, v135
	v_exp_f32_e32 v80, v88
	v_exp_f32_e32 v81, v89
	v_mfma_f32_32x32x16_bf16 v[112:127], a[196:199], a[132:135], v[112:127]
	ds_read_b64_tr_b16 v[186:187], v208 offset:0xc00
	v_cvt_pk_bf16_f32 v160, v136, v137
	v_exp_f32_e32 v90, v90
	v_exp_f32_e32 v91, v91
	v_mfma_f32_32x32x16_bf16 v[96:111], a[196:199], a[164:167], v[96:111]
	ds_read_b64_tr_b16 v[192:193], v208 offset:0x600
	v_cvt_pk_bf16_f32 v161, v138, v139
	v_exp_f32_e32 v232, v92
	v_exp_f32_e32 v233, v93
	v_mfma_f32_32x32x16_bf16 v[48:63], a[228:231], a[132:135], v[48:63]
	ds_read_b64_tr_b16 v[194:195], v208 offset:0xe00
	v_cvt_pk_bf16_f32 v162, v140, v141
	v_mfma_f32_32x32x16_bf16 v[32:47], a[228:231], a[164:167], v[32:47]
	ds_read_b64_tr_b16 v[188:189], v208 offset:0x1000
	v_exp_f32_e32 v234, v94
	v_exp_f32_e32 v235, v95
	ds_read_b64_tr_b16 v[190:191], v208 offset:0x1800
	v_cvt_pk_bf16_f32 v163, v142, v143
	v_exp_f32_e32 v130, v64
	v_exp_f32_e32 v131, v65
	v_mfma_f32_32x32x16_bf16 v[112:127], a[200:203], a[136:139], v[112:127]
	ds_read_b64_tr_b16 v[172:173], v208 offset:0x1200
	v_cvt_pk_bf16_f32 v196, v144, v145
	v_exp_f32_e32 v138, v66
	v_exp_f32_e32 v139, v67
	v_mfma_f32_32x32x16_bf16 v[96:111], a[200:203], a[168:171], v[96:111]
	ds_read_b64_tr_b16 v[174:175], v208 offset:0x1a00
	v_cvt_pk_bf16_f32 v197, v146, v147
	v_mfma_f32_32x32x16_bf16 v[48:63], a[232:235], a[136:139], v[48:63]
	ds_read_b64_tr_b16 v[164:165], v208 offset:0x1400
	v_exp_f32_e32 v242, v68
	v_exp_f32_e32 v243, v69
	v_cvt_pk_bf16_f32 v198, v148, v149
	v_mfma_f32_32x32x16_bf16 v[32:47], a[232:235], a[168:171], v[32:47]
	ds_read_b64_tr_b16 v[166:167], v208 offset:0x1c00
	ds_read_b64_tr_b16 v[144:145], v208 offset:0x1600
	v_exp_f32_e32 v244, v70
	v_exp_f32_e32 v245, v71
	v_cvt_pk_bf16_f32 v199, v150, v151
	v_exp_f32_e32 v64, v72
	v_exp_f32_e32 v65, v73
	v_mfma_f32_32x32x16_bf16 v[112:127], a[204:207], a[140:143], v[112:127]
	ds_read_b64_tr_b16 v[146:147], v208 offset:0x1e00
	v_cvt_pk_bf16_f32 v148, v152, v153
	v_exp_f32_e32 v70, v74
	v_exp_f32_e32 v71, v75
	v_mfma_f32_32x32x16_bf16 v[96:111], a[204:207], a[172:175], v[96:111]
	ds_read_b64_tr_b16 v[140:141], v208 offset:0x2000
	v_cvt_pk_bf16_f32 v149, v154, v155
	v_exp_f32_e32 v152, v76
	v_exp_f32_e32 v153, v77
	v_mfma_f32_32x32x16_bf16 v[48:63], a[236:239], a[140:143], v[48:63]
	ds_read_b64_tr_b16 v[142:143], v208 offset:0x2800
	v_cvt_pk_bf16_f32 v150, v156, v157
	v_mfma_f32_32x32x16_bf16 v[32:47], a[236:239], a[172:175], v[32:47]
	ds_read_b64_tr_b16 v[66:67], v208 offset:0x2200
	v_exp_f32_e32 v154, v78
	v_exp_f32_e32 v155, v79
	ds_read_b64_tr_b16 v[68:69], v208 offset:0x2a00
	v_cvt_pk_bf16_f32 v151, v158, v159
	s_mov_b32 s0, s51
	v_mfma_f32_32x32x16_bf16 v[112:127], a[208:211], a[144:147], v[112:127]
	ds_read_b64_tr_b16 v[132:133], v208 offset:0x2400
	v_cvt_pk_bf16_f32 v72, v240, v241
	v_add_f32_e32 v74, v237, v240
	v_add_f32_e32 v75, v236, v241
	s_mov_b32 s1, s72
	v_mfma_f32_32x32x16_bf16 v[96:111], a[208:211], a[176:179], v[96:111]
	ds_read_b64_tr_b16 v[134:135], v208 offset:0x2c00
	v_cvt_pk_bf16_f32 v73, v82, v83
	v_add_f32_e32 v78, v74, v82
	v_add_f32_e32 v75, v75, v83
	s_mov_b32 s4, s53
	v_mfma_f32_32x32x16_bf16 v[48:63], a[240:243], a[144:147], v[48:63]
	ds_read_b64_tr_b16 v[76:77], v208 offset:0x2600
	v_cvt_pk_bf16_f32 v74, v84, v85
	v_add_f32_e32 v84, v78, v84
	v_add_f32_e32 v85, v75, v85
	s_mov_b32 s5, s73
	v_mfma_f32_32x32x16_bf16 v[32:47], a[240:243], a[176:179], v[32:47]
	ds_read_b64_tr_b16 v[78:79], v208 offset:0x2e00
	ds_read_b64_tr_b16 v[82:83], v208 offset:0x3000
	v_cvt_pk_bf16_f32 v75, v86, v87
	v_add_f32_e32 v86, v84, v86
	v_add_f32_e32 v87, v85, v87
	s_mov_b32 s6, s55
	v_mfma_f32_32x32x16_bf16 v[112:127], a[212:215], a[148:151], v[112:127]
	ds_read_b64_tr_b16 v[84:85], v208 offset:0x3800
	v_add_f32_e32 v88, v86, v80
	v_add_f32_e32 v89, v87, v81
	s_mov_b32 s16, s74
	v_mfma_f32_32x32x16_bf16 v[96:111], a[212:215], a[180:183], v[96:111]
	ds_read_b64_tr_b16 v[86:87], v208 offset:0x3200
	v_add_f32_e32 v92, v88, v90
	v_add_f32_e32 v93, v89, v91
	s_mov_b32 s17, s57
	v_mfma_f32_32x32x16_bf16 v[48:63], a[244:247], a[148:151], v[48:63]
	ds_read_b64_tr_b16 v[88:89], v208 offset:0x3a00
	v_add_f32_e32 v128, v92, v232
	v_add_f32_e32 v129, v93, v233
	s_mov_b32 s19, s75
	v_mfma_f32_32x32x16_bf16 v[32:47], a[244:247], a[180:183], v[32:47]
	ds_read_b64_tr_b16 v[92:93], v208 offset:0x3400
	ds_read_b64_tr_b16 v[94:95], v208 offset:0x3c00
	v_add_f32_e32 v156, v128, v234
	v_add_f32_e32 v157, v129, v235
	s_mov_b32 s20, s31
	v_mfma_f32_32x32x16_bf16 v[112:127], a[216:219], a[152:155], v[112:127]
	ds_read_b64_tr_b16 v[128:129], v208 offset:0x3600
	v_cvt_pk_bf16_f32 v136, v130, v131
	v_add_f32_e32 v158, v238, v130
	v_add_f32_e32 v159, v239, v131
	s_mov_b32 s21, s64
	v_mfma_f32_32x32x16_bf16 v[96:111], a[216:219], a[184:187], v[96:111]
	ds_read_b64_tr_b16 v[130:131], v208 offset:0x3e00
	v_cvt_pk_bf16_f32 v137, v138, v139
	v_add_f32_e32 v158, v158, v138
	v_add_f32_e32 v139, v159, v139
	v_mfma_f32_32x32x16_bf16 v[48:63], a[248:251], a[152:155], v[48:63]
	s_mov_b32 s22, s59
	v_cvt_pk_bf16_f32 v138, v242, v243
	v_add_f32_e32 v158, v158, v242
	v_add_f32_e32 v159, v139, v243
	v_mfma_f32_32x32x16_bf16 v[32:47], a[248:251], a[184:187], v[32:47]
	s_mov_b32 s23, s76
	v_cvt_pk_bf16_f32 v139, v244, v245
	v_add_f32_e32 v158, v158, v244
	v_add_f32_e32 v159, v159, v245
	v_mfma_f32_32x32x16_bf16 v[112:127], a[220:223], a[156:159], v[112:127]
	s_mov_b32 s24, s61
	v_add_f32_e32 v158, v158, v64
	v_add_f32_e32 v159, v159, v65
	v_mfma_f32_32x32x16_bf16 v[96:111], a[220:223], a[188:191], v[96:111]
	s_mov_b32 s81, s66
	v_add_f32_e32 v158, v158, v70
	v_add_f32_e32 v159, v159, v71
	v_mfma_f32_32x32x16_bf16 v[48:63], a[252:255], a[156:159], v[48:63]
	s_mov_b32 s82, s62
	v_add_f32_e32 v158, v158, v152
	v_add_f32_e32 v159, v159, v153
	v_mfma_f32_32x32x16_bf16 v[32:47], a[252:255], a[188:191], v[32:47]
	s_mov_b32 s83, s77
	v_add_f32_e32 v158, v158, v154
	v_add_f32_e32 v159, v159, v155
	s_nop 4
	v_add_f32_e32 v156, v156, v157
	s_waitcnt vmcnt(0) lgkmcnt(0)
	s_barrier
	s_nop 0
	v_mov_b32_e32 v157, v156
	s_nop 1
	v_permlane32_swap_b32_e32 v156, v157
	v_add_f32_e32 v156, v156, v157
	v_add_f32_e32 v231, v231, v156
	v_add_f32_e32 v156, v158, v159
	v_mov_b32_e32 v157, v156
	s_nop 1
	v_permlane32_swap_b32_e32 v156, v157
	v_add_f32_e32 v156, v156, v157
	v_add_f32_e32 v230, v230, v156
	s_nop 1
	v_mfma_f32_32x32x16_bf16 a[0:15], v[176:179], v[168:171], a[0:15]
	v_mfma_f32_32x32x16_bf16 a[16:31], v[176:179], v[196:199], a[16:31]
	v_mfma_f32_32x32x16_bf16 a[32:47], v[180:183], v[168:171], a[32:47]
	v_mfma_f32_32x32x16_bf16 a[48:63], v[180:183], v[196:199], a[48:63]
	v_mfma_f32_32x32x16_bf16 a[64:79], v[184:187], v[168:171], a[64:79]
	v_mfma_f32_32x32x16_bf16 a[80:95], v[184:187], v[196:199], a[80:95]
	v_mfma_f32_32x32x16_bf16 a[96:111], v[192:195], v[168:171], a[96:111]
	v_mfma_f32_32x32x16_bf16 a[112:127], v[192:195], v[196:199], a[112:127]
	v_mfma_f32_32x32x16_bf16 a[0:15], v[188:191], v[160:163], a[0:15]
	v_max3_f32 v156, v112, v113, v48
	v_max3_f32 v157, v114, v115, v49
	v_max3_f32 v156, v156, v50, v51
	v_mfma_f32_32x32x16_bf16 a[16:31], v[188:191], v[148:151], a[16:31]
	v_max3_f32 v156, v156, v116, v117
	v_max3_f32 v157, v157, v118, v119
	v_max3_f32 v156, v156, v52, v53
	v_max3_f32 v157, v157, v54, v55
	v_mfma_f32_32x32x16_bf16 a[32:47], v[172:175], v[160:163], a[32:47]
	v_max3_f32 v156, v156, v120, v121
	v_max3_f32 v157, v157, v122, v123
	v_max3_f32 v156, v156, v56, v57
	v_max3_f32 v157, v157, v58, v59
	v_mfma_f32_32x32x16_bf16 a[48:63], v[172:175], v[148:151], a[48:63]
	v_max3_f32 v156, v156, v124, v125
	v_max3_f32 v157, v157, v126, v127
	v_max3_f32 v156, v156, v60, v61
	v_max3_f32 v157, v157, v62, v63
	v_mfma_f32_32x32x16_bf16 a[64:79], v[164:167], v[160:163], a[64:79]
	v_max3_f32 v158, v96, v97, v32
	v_max3_f32 v159, v98, v99, v33
	v_max3_f32 v158, v158, v34, v35
	v_mfma_f32_32x32x16_bf16 a[80:95], v[164:167], v[148:151], a[80:95]
	v_max3_f32 v158, v158, v100, v101
	v_max3_f32 v159, v159, v102, v103
	v_max3_f32 v158, v158, v36, v37
	v_max3_f32 v159, v159, v38, v39
	v_mfma_f32_32x32x16_bf16 a[96:111], v[144:147], v[160:163], a[96:111]
	v_max3_f32 v158, v158, v104, v105
	v_max3_f32 v159, v159, v106, v107
	v_max3_f32 v158, v158, v40, v41
	v_max3_f32 v159, v159, v42, v43
	v_mfma_f32_32x32x16_bf16 a[112:127], v[144:147], v[148:151], a[112:127]
	v_max3_f32 v145, v159, v110, v111
	v_max3_f32 v144, v158, v108, v109
	v_max3_f32 v146, v144, v44, v45
	v_max3_f32 v145, v145, v46, v47
	v_mfma_f32_32x32x16_bf16 a[0:15], v[140:143], v[72:75], a[0:15]
	v_max_f32_e32 v144, v156, v157
	v_mov_b32_e32 v147, v144
	s_nop 1
	v_permlane32_swap_b32_e32 v144, v147
	v_max_f32_e32 v144, v144, v147
	v_mfma_f32_32x32x16_bf16 a[16:31], v[140:143], v[136:139], a[16:31]
	v_max_f32_e32 v140, v146, v145
	v_mov_b32_e32 v141, v140
	s_nop 1
	v_permlane32_swap_b32_e32 v140, v141
	v_max_f32_e32 v140, v140, v141
	v_max_f32_e32 v141, v144, v144
	v_max_f32_e32 v142, v140, v140
	v_max_f32_e32 v141, v141, v142
	v_mfma_f32_32x32x16_bf16 a[32:47], v[66:69], v[72:75], a[32:47]
	v_cmp_lt_f32_e32 vcc, s79, v141
	s_cmp_lg_u64 vcc, 0
	s_cselect_b64 s[0:1], -1, 0
	s_cbranch_vccnz .LBB2_62
.LBB2_25:
	v_cvt_pk_bf16_f32 v140, v80, v81
	v_cvt_pk_bf16_f32 v141, v90, v91
	v_cvt_pk_bf16_f32 v142, v232, v233
	v_cvt_pk_bf16_f32 v143, v234, v235
	v_cvt_pk_bf16_f32 v144, v64, v65
	v_cvt_pk_bf16_f32 v145, v70, v71
	v_cvt_pk_bf16_f32 v146, v152, v153
	v_cvt_pk_bf16_f32 v147, v154, v155
	v_exp_f32_e32 v64, v112
	v_exp_f32_e32 v65, v113
	v_mfma_f32_32x32x16_bf16 a[48:63], v[66:69], v[136:139], a[48:63]
	v_exp_f32_e32 v66, v114
	v_exp_f32_e32 v67, v115
	v_mfma_f32_32x32x16_bf16 a[64:79], v[132:135], v[72:75], a[64:79]
	v_add_f32_e32 v71, v201, v64
	v_add_f32_e32 v80, v201, v65
	v_exp_f32_e32 v68, v116
	v_exp_f32_e32 v69, v117
	v_exp_f32_e32 v70, v118
	v_mfma_f32_32x32x16_bf16 a[80:95], v[132:135], v[136:139], a[80:95]
	v_add_f32_e32 v81, v71, v66
	v_add_f32_e32 v80, v80, v67
	v_mfma_f32_32x32x16_bf16 a[96:111], v[76:79], v[72:75], a[96:111]
	v_exp_f32_e32 v71, v119
	v_exp_f32_e32 v72, v120
	v_add_f32_e32 v73, v81, v68
	v_add_f32_e32 v80, v80, v69
	v_add_f32_e32 v81, v73, v70
	v_exp_f32_e32 v73, v121
	v_exp_f32_e32 v74, v122
	v_exp_f32_e32 v75, v123
	v_mfma_f32_32x32x16_bf16 a[112:127], v[76:79], v[136:139], a[112:127]
	v_add_f32_e32 v78, v80, v71
	v_add_f32_e32 v79, v81, v72
	v_exp_f32_e32 v76, v124
	v_exp_f32_e32 v77, v125
	v_mfma_f32_32x32x16_bf16 a[0:15], v[82:85], v[140:143], a[0:15]
	v_add_f32_e32 v78, v78, v73
	v_add_f32_e32 v81, v79, v74
	v_add_f32_e32 v90, v78, v75
	v_exp_f32_e32 v78, v126
	v_exp_f32_e32 v79, v127
	v_exp_f32_e32 v80, v96
	v_mfma_f32_32x32x16_bf16 a[16:31], v[82:85], v[144:147], a[16:31]
	v_add_f32_e32 v83, v81, v76
	v_add_f32_e32 v84, v90, v77
	v_exp_f32_e32 v81, v97
	v_exp_f32_e32 v82, v98
	v_mfma_f32_32x32x16_bf16 a[32:47], v[86:89], v[140:143], a[32:47]
	v_add_f32_e32 v161, v83, v78
	v_add_f32_e32 v160, v84, v79
	v_add_f32_e32 v90, v201, v80
	v_exp_f32_e32 v83, v99
	v_exp_f32_e32 v84, v100
	v_exp_f32_e32 v85, v101
	v_mfma_f32_32x32x16_bf16 a[48:63], v[86:89], v[144:147], a[48:63]
	v_add_f32_e32 v88, v201, v81
	v_add_f32_e32 v89, v90, v82
	v_exp_f32_e32 v86, v102
	v_exp_f32_e32 v87, v103
	v_mfma_f32_32x32x16_bf16 a[64:79], v[92:95], v[140:143], a[64:79]
	v_add_f32_e32 v88, v88, v83
	v_add_f32_e32 v91, v89, v84
	v_add_f32_e32 v96, v88, v85
	v_exp_f32_e32 v88, v104
	v_exp_f32_e32 v89, v105
	v_exp_f32_e32 v90, v106
	v_mfma_f32_32x32x16_bf16 a[80:95], v[92:95], v[144:147], a[80:95]
	v_add_f32_e32 v93, v91, v86
	v_add_f32_e32 v94, v96, v87
	v_exp_f32_e32 v91, v107
	v_exp_f32_e32 v92, v108
	v_mfma_f32_32x32x16_bf16 a[96:111], v[128:131], v[140:143], a[96:111]
	v_add_f32_e32 v93, v93, v88
	v_add_f32_e32 v96, v94, v89
	v_add_f32_e32 v97, v93, v90
	v_exp_f32_e32 v93, v109
	v_exp_f32_e32 v94, v110
	v_exp_f32_e32 v95, v111
	v_mfma_f32_32x32x16_bf16 a[112:127], v[128:131], v[144:147], a[112:127]
	v_add_f32_e32 v96, v96, v91
	v_add_f32_e32 v97, v97, v92
	s_andn2_b64 vcc, exec, s[0:1]
	v_add_f32_e32 v96, v96, v93
	v_add_f32_e32 v162, v97, v94
	s_nop 0
	v_add_f32_e32 v163, v96, v95
	s_cbranch_vccz .LBB2_63
.LBB2_26:
	s_waitcnt lgkmcnt(0)
	ds_read_b64_tr_b16 v[156:157], v223 offset:0
	ds_read_b64_tr_b16 v[158:159], v223 offset:0x800
	ds_read_b64_tr_b16 v[152:153], v223 offset:0x200
	ds_read_b64_tr_b16 v[154:155], v223 offset:0xa00
	ds_read_b64_tr_b16 v[148:149], v223 offset:0x400
	ds_read_b64_tr_b16 v[150:151], v223 offset:0xc00
	ds_read_b64_tr_b16 v[144:145], v223 offset:0x600
	ds_read_b64_tr_b16 v[146:147], v223 offset:0xe00
	ds_read_b64_tr_b16 v[140:141], v223 offset:0x1000
	ds_read_b64_tr_b16 v[142:143], v223 offset:0x1800
	ds_read_b64_tr_b16 v[136:137], v223 offset:0x1200
	ds_read_b64_tr_b16 v[138:139], v223 offset:0x1a00
	ds_read_b64_tr_b16 v[132:133], v223 offset:0x1400
	ds_read_b64_tr_b16 v[134:135], v223 offset:0x1c00
	ds_read_b64_tr_b16 v[128:129], v223 offset:0x1600
	ds_read_b64_tr_b16 v[130:131], v223 offset:0x1e00
	ds_read_b64_tr_b16 v[124:125], v223 offset:0x2000
	ds_read_b64_tr_b16 v[126:127], v223 offset:0x2800
	v_exp_f32_e32 v48, v48
	v_exp_f32_e32 v49, v49
	ds_read_b64_tr_b16 v[120:121], v223 offset:0x2200
	ds_read_b64_tr_b16 v[122:123], v223 offset:0x2a00
	ds_read_b64_tr_b16 v[116:117], v223 offset:0x2400
	ds_read_b64_tr_b16 v[118:119], v223 offset:0x2c00
	v_exp_f32_e32 v190, v44
	v_cvt_pk_bf16_f32 v44, v48, v49
	v_add_f32_e32 v48, v161, v48
	v_add_f32_e32 v49, v160, v49
	ds_read_b64_tr_b16 v[112:113], v223 offset:0x2600
	v_exp_f32_e32 v164, v50
	v_exp_f32_e32 v165, v51
	v_add_f32_e32 v48, v48, v164
	v_add_f32_e32 v49, v49, v165
	ds_read_b64_tr_b16 v[114:115], v223 offset:0x2e00
	v_exp_f32_e32 v166, v52
	v_exp_f32_e32 v167, v53
	v_add_f32_e32 v48, v48, v166
	v_add_f32_e32 v49, v49, v167
	ds_read_b64_tr_b16 v[108:109], v223 offset:0x3000
	v_exp_f32_e32 v168, v54
	v_exp_f32_e32 v169, v55
	v_exp_f32_e32 v178, v32
	v_cvt_pk_bf16_f32 v51, v66, v67
	v_add_f32_e32 v48, v48, v168
	v_add_f32_e32 v49, v49, v169
	v_add_f32_e32 v66, v162, v178
	ds_read_b64_tr_b16 v[110:111], v223 offset:0x3800
	v_exp_f32_e32 v170, v56
	v_exp_f32_e32 v171, v57
	v_exp_f32_e32 v179, v33
	v_exp_f32_e32 v180, v34
	v_add_f32_e32 v48, v48, v170
	v_add_f32_e32 v49, v49, v171
	v_add_f32_e32 v67, v163, v179
	v_add_f32_e32 v66, v66, v180
	ds_read_b64_tr_b16 v[104:105], v223 offset:0x3200
	v_exp_f32_e32 v172, v58
	v_exp_f32_e32 v173, v59
	v_exp_f32_e32 v181, v35
	v_exp_f32_e32 v182, v36
	v_add_f32_e32 v48, v48, v172
	v_add_f32_e32 v49, v49, v173
	v_add_f32_e32 v67, v67, v181
	v_add_f32_e32 v66, v66, v182
	ds_read_b64_tr_b16 v[106:107], v223 offset:0x3a00
	v_exp_f32_e32 v174, v60
	v_exp_f32_e32 v175, v61
	v_exp_f32_e32 v183, v37
	v_exp_f32_e32 v184, v38
	v_add_f32_e32 v48, v48, v174
	v_add_f32_e32 v49, v49, v175
	v_add_f32_e32 v67, v67, v183
	v_add_f32_e32 v66, v66, v184
	ds_read_b64_tr_b16 v[100:101], v223 offset:0x3400
	v_exp_f32_e32 v176, v62
	v_exp_f32_e32 v177, v63
	v_exp_f32_e32 v185, v39
	v_exp_f32_e32 v186, v40
	v_add_f32_e32 v48, v48, v176
	v_add_f32_e32 v49, v49, v177
	v_add_f32_e32 v67, v67, v185
	v_add_f32_e32 v66, v66, v186
	ds_read_b64_tr_b16 v[102:103], v223 offset:0x3c00
	v_exp_f32_e32 v187, v41
	v_exp_f32_e32 v188, v42
	v_add_f32_e32 v67, v67, v187
	v_add_f32_e32 v66, v66, v188
	v_add_f32_e32 v48, v48, v49
	ds_read_b64_tr_b16 v[96:97], v223 offset:0x3600
	v_exp_f32_e32 v189, v43
	v_mov_b32_e32 v49, v48
	v_exp_f32_e32 v191, v45
	v_exp_f32_e32 v192, v46
	v_exp_f32_e32 v193, v47
	v_add_f32_e32 v67, v67, v189
	v_add_f32_e32 v66, v66, v190
	v_permlane32_swap_b32_e32 v48, v49
	ds_read_b64_tr_b16 v[98:99], v223 offset:0x3e00
	s_nop 1
	s_nop 1
	s_nop 1
	s_nop 1
	s_nop 1
	s_nop 1
	s_nop 1
	s_nop 1
	s_nop 1
	s_nop 1
	s_nop 1
	s_nop 1
	s_nop 1
	s_nop 1
	v_add_f32_e32 v67, v67, v191
	s_nop 1
	v_add_f32_e32 v66, v66, v192
	s_nop 1
	v_add_f32_e32 v48, v48, v49
	s_waitcnt lgkmcnt(0)
	s_nop 0
	v_cvt_pk_bf16_f32 v50, v64, v65
	v_add_f32_e32 v67, v67, v193
	v_add_f32_e32 v49, v231, v48
	v_cvt_pk_bf16_f32 v52, v68, v69
	v_add_f32_e32 v48, v66, v67
	v_cvt_pk_bf16_f32 v36, v72, v73
	v_mov_b32_e32 v66, v48
	s_nop 1
	v_permlane32_swap_b32_e32 v48, v66
	v_cvt_pk_bf16_f32 v37, v74, v75
	v_cvt_pk_bf16_f32 v38, v76, v77
	v_cvt_pk_bf16_f32 v39, v78, v79
	v_cvt_pk_bf16_f32 v45, v164, v165
	v_cvt_pk_bf16_f32 v46, v166, v167
	v_cvt_pk_bf16_f32 v47, v168, v169
	v_cvt_pk_bf16_f32 v32, v170, v171
	v_cvt_pk_bf16_f32 v33, v172, v173
	v_cvt_pk_bf16_f32 v34, v174, v175
	v_cvt_pk_bf16_f32 v35, v176, v177
	v_cvt_pk_bf16_f32 v40, v186, v187
	v_cvt_pk_bf16_f32 v41, v188, v189
	v_cvt_pk_bf16_f32 v42, v190, v191
	v_cvt_pk_bf16_f32 v43, v192, v193
	v_add_f32_e32 v48, v48, v66
	v_cvt_pk_bf16_f32 v53, v70, v71
	v_cvt_pk_bf16_f32 v54, v80, v81
	v_cvt_pk_bf16_f32 v55, v82, v83
	v_cvt_pk_bf16_f32 v56, v84, v85
	v_cvt_pk_bf16_f32 v57, v86, v87
	v_cvt_pk_bf16_f32 v58, v88, v89
	v_cvt_pk_bf16_f32 v59, v90, v91
	v_cvt_pk_bf16_f32 v60, v92, v93
	v_cvt_pk_bf16_f32 v61, v94, v95
	v_cvt_pk_bf16_f32 v62, v178, v179
	v_cvt_pk_bf16_f32 v63, v180, v181
	v_cvt_pk_bf16_f32 v64, v182, v183
	v_cvt_pk_bf16_f32 v65, v184, v185
	v_add_f32_e32 v48, v230, v48
	s_nop 1
	v_mfma_f32_32x32x16_bf16 a[0:15], v[156:159], v[50:53], a[0:15]
	v_mfma_f32_32x32x16_bf16 a[16:31], v[156:159], v[54:57], a[16:31]
	v_mfma_f32_32x32x16_bf16 a[32:47], v[152:155], v[50:53], a[32:47]
	v_mfma_f32_32x32x16_bf16 a[48:63], v[152:155], v[54:57], a[48:63]
	v_mfma_f32_32x32x16_bf16 a[64:79], v[148:151], v[50:53], a[64:79]
	v_mfma_f32_32x32x16_bf16 a[80:95], v[148:151], v[54:57], a[80:95]
	v_mfma_f32_32x32x16_bf16 a[96:111], v[144:147], v[50:53], a[96:111]
	v_mfma_f32_32x32x16_bf16 a[112:127], v[144:147], v[54:57], a[112:127]
	v_mfma_f32_32x32x16_bf16 a[0:15], v[140:143], v[36:39], a[0:15]
	v_mfma_f32_32x32x16_bf16 a[16:31], v[140:143], v[58:61], a[16:31]
	v_mfma_f32_32x32x16_bf16 a[32:47], v[136:139], v[36:39], a[32:47]
	v_mfma_f32_32x32x16_bf16 a[48:63], v[136:139], v[58:61], a[48:63]
	v_mfma_f32_32x32x16_bf16 a[64:79], v[132:135], v[36:39], a[64:79]
	v_mfma_f32_32x32x16_bf16 a[80:95], v[132:135], v[58:61], a[80:95]
	v_mfma_f32_32x32x16_bf16 a[96:111], v[128:131], v[36:39], a[96:111]
	v_mfma_f32_32x32x16_bf16 a[112:127], v[128:131], v[58:61], a[112:127]
	v_mfma_f32_32x32x16_bf16 a[0:15], v[124:127], v[44:47], a[0:15]
	v_mfma_f32_32x32x16_bf16 a[16:31], v[124:127], v[62:65], a[16:31]
	v_mfma_f32_32x32x16_bf16 a[32:47], v[120:123], v[44:47], a[32:47]
	v_mfma_f32_32x32x16_bf16 a[48:63], v[120:123], v[62:65], a[48:63]
	v_mfma_f32_32x32x16_bf16 a[64:79], v[116:119], v[44:47], a[64:79]
	v_mfma_f32_32x32x16_bf16 a[80:95], v[116:119], v[62:65], a[80:95]
	v_mfma_f32_32x32x16_bf16 a[96:111], v[112:115], v[44:47], a[96:111]
	v_mfma_f32_32x32x16_bf16 a[112:127], v[112:115], v[62:65], a[112:127]
	v_mfma_f32_32x32x16_bf16 a[0:15], v[108:111], v[32:35], a[0:15]
	v_mfma_f32_32x32x16_bf16 a[16:31], v[108:111], v[40:43], a[16:31]
	v_mfma_f32_32x32x16_bf16 a[32:47], v[104:107], v[32:35], a[32:47]
	v_mfma_f32_32x32x16_bf16 a[48:63], v[104:107], v[40:43], a[48:63]
	v_mfma_f32_32x32x16_bf16 a[64:79], v[100:103], v[32:35], a[64:79]
	v_mfma_f32_32x32x16_bf16 a[80:95], v[100:103], v[40:43], a[80:95]
	v_mfma_f32_32x32x16_bf16 a[96:111], v[96:99], v[32:35], a[96:111]
	v_mfma_f32_32x32x16_bf16 a[112:127], v[96:99], v[40:43], a[112:127]
	v_rcp_f32_e32 v34, v49
	s_nop 7
	s_nop 7
	v_mov_b32_e32 v132, v48
	v_cmp_lt_f32_e32 vcc, 0, v49
	v_cndmask_b32_e32 v43, 0, v34, vcc
	v_lshrrev_b32_e32 v42, 4, v225
	s_lshl_b32 s4, s26, 11
	v_mov_b32_e32 v33, s29
	v_or_b32_e32 v32, s28, v200
	s_and_b32 s24, s4, 0x3800
	v_lshl_add_u64 v[34:35], s[24:25], 0, v[32:33]
	v_lshlrev_b32_e32 v39, 8, v42
	v_lshlrev_b32_e32 v32, 4, v225
	v_and_or_b32 v200, v32, s80, v39
	v_lshl_add_u64 v[32:33], s[14:15], 0, v[200:201]
	v_lshlrev_b64 v[34:35], 8, v[34:35]
	v_lshl_add_u64 v[124:125], v[32:33], 0, v[34:35]
	v_mov_b32_e32 v34, 0x1000
	v_mov_b32_e32 v35, 0
	v_lshl_add_u64 v[126:127], v[124:125], 0, v[34:35]
	v_lshl_add_u64 v[128:129], v[126:127], 0, v[34:35]
	v_lshl_add_u64 v[130:131], v[128:129], 0, v[34:35]
	v_and_b32_e32 v32, 31, v225
	v_lshl_add_u32 v36, v32, 8, v214
	v_and_b32_e32 v37, 15, v225
	v_lshlrev_b32_e32 v37, 4, v37
	v_lshrrev_b32_e32 v38, 5, v225
	v_lshlrev_b32_e32 v38, 3, v38
	v_xad_u32 v100, v38, v37, v36
	v_add_u32_e32 v101, 0x10, v38
	v_xad_u32 v101, v101, v37, v36
	v_add_u32_e32 v102, 0x20, v38
	v_xad_u32 v102, v102, v37, v36
	v_add_u32_e32 v103, 0x30, v38
	v_xad_u32 v103, v103, v37, v36
	v_add_u32_e32 v104, 0x40, v38
	v_xad_u32 v104, v104, v37, v36
	v_add_u32_e32 v105, 0x50, v38
	v_xad_u32 v105, v105, v37, v36
	v_add_u32_e32 v106, 0x60, v38
	v_xad_u32 v106, v106, v37, v36
	v_add_u32_e32 v107, 0x70, v38
	v_xad_u32 v107, v107, v37, v36
	v_add_u32_e32 v108, 0x80, v38
	v_xad_u32 v108, v108, v37, v36
	v_add_u32_e32 v109, 0x90, v38
	v_xad_u32 v109, v109, v37, v36
	v_add_u32_e32 v110, 0xa0, v38
	v_xad_u32 v110, v110, v37, v36
	v_add_u32_e32 v111, 0xb0, v38
	v_xad_u32 v111, v111, v37, v36
	v_add_u32_e32 v112, 0xc0, v38
	v_xad_u32 v112, v112, v37, v36
	v_add_u32_e32 v113, 0xd0, v38
	v_xad_u32 v113, v113, v37, v36
	v_add_u32_e32 v114, 0xe0, v38
	v_xad_u32 v114, v114, v37, v36
	v_add_u32_e32 v115, 0xf0, v38
	v_xad_u32 v115, v115, v37, v36
	v_and_b32_e32 v33, 15, v225
	v_mov_b32_e32 v116, v42
	v_and_b32_e32 v39, 15, v116
	v_xor_b32_e32 v39, v39, v33
	v_lshlrev_b32_e32 v39, 4, v39
	v_lshl_add_u32 v116, v116, 8, v214
	v_add_u32_e32 v116, v116, v39
	v_add_u32_e32 v117, 4, v42
	v_and_b32_e32 v39, 15, v117
	v_xor_b32_e32 v39, v39, v33
	v_lshlrev_b32_e32 v39, 4, v39
	v_lshl_add_u32 v117, v117, 8, v214
	v_add_u32_e32 v117, v117, v39
	v_add_u32_e32 v118, 8, v42
	v_and_b32_e32 v39, 15, v118
	v_xor_b32_e32 v39, v39, v33
	v_lshlrev_b32_e32 v39, 4, v39
	v_lshl_add_u32 v118, v118, 8, v214
	v_add_u32_e32 v118, v118, v39
	v_add_u32_e32 v119, 12, v42
	v_and_b32_e32 v39, 15, v119
	v_xor_b32_e32 v39, v39, v33
	v_lshlrev_b32_e32 v39, 4, v39
	v_lshl_add_u32 v119, v119, 8, v214
	v_add_u32_e32 v119, v119, v39
	v_add_u32_e32 v120, 16, v42
	v_and_b32_e32 v39, 15, v120
	v_xor_b32_e32 v39, v39, v33
	v_lshlrev_b32_e32 v39, 4, v39
	v_lshl_add_u32 v120, v120, 8, v214
	v_add_u32_e32 v120, v120, v39
	v_add_u32_e32 v121, 20, v42
	v_and_b32_e32 v39, 15, v121
	v_xor_b32_e32 v39, v39, v33
	v_lshlrev_b32_e32 v39, 4, v39
	v_lshl_add_u32 v121, v121, 8, v214
	v_add_u32_e32 v121, v121, v39
	v_add_u32_e32 v122, 24, v42
	v_and_b32_e32 v39, 15, v122
	v_xor_b32_e32 v39, v39, v33
	v_lshlrev_b32_e32 v39, 4, v39
	v_lshl_add_u32 v122, v122, 8, v214
	v_add_u32_e32 v122, v122, v39
	v_add_u32_e32 v123, 28, v42
	v_and_b32_e32 v39, 15, v123
	v_xor_b32_e32 v39, v39, v33
	v_lshlrev_b32_e32 v39, 4, v39
	v_lshl_add_u32 v123, v123, 8, v214
	v_add_u32_e32 v123, v123, v39
	v_accvgpr_read_b32 v64, a0
	v_accvgpr_read_b32 v65, a1
	v_accvgpr_read_b32 v66, a2
	v_accvgpr_read_b32 v67, a3
	v_accvgpr_read_b32 v68, a4
	v_accvgpr_read_b32 v69, a5
	v_accvgpr_read_b32 v70, a6
	v_accvgpr_read_b32 v71, a7
	v_accvgpr_read_b32 v72, a8
	v_accvgpr_read_b32 v73, a9
	v_accvgpr_read_b32 v74, a10
	v_accvgpr_read_b32 v75, a11
	v_accvgpr_read_b32 v76, a12
	v_accvgpr_read_b32 v77, a13
	v_accvgpr_read_b32 v78, a14
	v_accvgpr_read_b32 v79, a15
	v_mul_f32_e32 v64, v64, v43
	v_mul_f32_e32 v65, v65, v43
	v_mul_f32_e32 v66, v66, v43
	v_mul_f32_e32 v67, v67, v43
	v_mul_f32_e32 v68, v68, v43
	v_mul_f32_e32 v69, v69, v43
	v_mul_f32_e32 v70, v70, v43
	v_mul_f32_e32 v71, v71, v43
	v_mul_f32_e32 v72, v72, v43
	v_mul_f32_e32 v73, v73, v43
	v_mul_f32_e32 v74, v74, v43
	v_mul_f32_e32 v75, v75, v43
	v_mul_f32_e32 v76, v76, v43
	v_mul_f32_e32 v77, v77, v43
	v_mul_f32_e32 v78, v78, v43
	v_mul_f32_e32 v79, v79, v43
	v_cvt_pk_f16_f32 v80, v64, v65
	v_cvt_pk_f16_f32 v81, v66, v67
	v_cvt_pk_f16_f32 v82, v68, v69
	v_cvt_pk_f16_f32 v83, v70, v71
	v_cvt_pk_f16_f32 v84, v72, v73
	v_cvt_pk_f16_f32 v85, v74, v75
	v_cvt_pk_f16_f32 v86, v76, v77
	v_cvt_pk_f16_f32 v87, v78, v79
	ds_write_b64 v100, v[80:81]
	ds_write_b64 v101, v[82:83]
	ds_write_b64 v102, v[84:85]
	ds_write_b64 v103, v[86:87]
	v_accvgpr_read_b32 v64, a32
	v_accvgpr_read_b32 v65, a33
	v_accvgpr_read_b32 v66, a34
	v_accvgpr_read_b32 v67, a35
	v_accvgpr_read_b32 v68, a36
	v_accvgpr_read_b32 v69, a37
	v_accvgpr_read_b32 v70, a38
	v_accvgpr_read_b32 v71, a39
	v_accvgpr_read_b32 v72, a40
	v_accvgpr_read_b32 v73, a41
	v_accvgpr_read_b32 v74, a42
	v_accvgpr_read_b32 v75, a43
	v_accvgpr_read_b32 v76, a44
	v_accvgpr_read_b32 v77, a45
	v_accvgpr_read_b32 v78, a46
	v_accvgpr_read_b32 v79, a47
	v_mul_f32_e32 v64, v64, v43
	v_mul_f32_e32 v65, v65, v43
	v_mul_f32_e32 v66, v66, v43
	v_mul_f32_e32 v67, v67, v43
	v_mul_f32_e32 v68, v68, v43
	v_mul_f32_e32 v69, v69, v43
	v_mul_f32_e32 v70, v70, v43
	v_mul_f32_e32 v71, v71, v43
	v_mul_f32_e32 v72, v72, v43
	v_mul_f32_e32 v73, v73, v43
	v_mul_f32_e32 v74, v74, v43
	v_mul_f32_e32 v75, v75, v43
	v_mul_f32_e32 v76, v76, v43
	v_mul_f32_e32 v77, v77, v43
	v_mul_f32_e32 v78, v78, v43
	v_mul_f32_e32 v79, v79, v43
	v_cvt_pk_f16_f32 v80, v64, v65
	v_cvt_pk_f16_f32 v81, v66, v67
	v_cvt_pk_f16_f32 v82, v68, v69
	v_cvt_pk_f16_f32 v83, v70, v71
	v_cvt_pk_f16_f32 v84, v72, v73
	v_cvt_pk_f16_f32 v85, v74, v75
	v_cvt_pk_f16_f32 v86, v76, v77
	v_cvt_pk_f16_f32 v87, v78, v79
	ds_write_b64 v104, v[80:81]
	ds_write_b64 v105, v[82:83]
	ds_write_b64 v106, v[84:85]
	ds_write_b64 v107, v[86:87]
	v_accvgpr_read_b32 v64, a64
	v_accvgpr_read_b32 v65, a65
	v_accvgpr_read_b32 v66, a66
	v_accvgpr_read_b32 v67, a67
	v_accvgpr_read_b32 v68, a68
	v_accvgpr_read_b32 v69, a69
	v_accvgpr_read_b32 v70, a70
	v_accvgpr_read_b32 v71, a71
	v_accvgpr_read_b32 v72, a72
	v_accvgpr_read_b32 v73, a73
	v_accvgpr_read_b32 v74, a74
	v_accvgpr_read_b32 v75, a75
	v_accvgpr_read_b32 v76, a76
	v_accvgpr_read_b32 v77, a77
	v_accvgpr_read_b32 v78, a78
	v_accvgpr_read_b32 v79, a79
	v_mul_f32_e32 v64, v64, v43
	v_mul_f32_e32 v65, v65, v43
	v_mul_f32_e32 v66, v66, v43
	v_mul_f32_e32 v67, v67, v43
	v_mul_f32_e32 v68, v68, v43
	v_mul_f32_e32 v69, v69, v43
	v_mul_f32_e32 v70, v70, v43
	v_mul_f32_e32 v71, v71, v43
	v_mul_f32_e32 v72, v72, v43
	v_mul_f32_e32 v73, v73, v43
	v_mul_f32_e32 v74, v74, v43
	v_mul_f32_e32 v75, v75, v43
	v_mul_f32_e32 v76, v76, v43
	v_mul_f32_e32 v77, v77, v43
	v_mul_f32_e32 v78, v78, v43
	v_mul_f32_e32 v79, v79, v43
	v_cvt_pk_f16_f32 v80, v64, v65
	v_cvt_pk_f16_f32 v81, v66, v67
	v_cvt_pk_f16_f32 v82, v68, v69
	v_cvt_pk_f16_f32 v83, v70, v71
	v_cvt_pk_f16_f32 v84, v72, v73
	v_cvt_pk_f16_f32 v85, v74, v75
	v_cvt_pk_f16_f32 v86, v76, v77
	v_cvt_pk_f16_f32 v87, v78, v79
	ds_write_b64 v108, v[80:81]
	ds_write_b64 v109, v[82:83]
	ds_write_b64 v110, v[84:85]
	ds_write_b64 v111, v[86:87]
	v_accvgpr_read_b32 v64, a96
	v_accvgpr_read_b32 v65, a97
	v_accvgpr_read_b32 v66, a98
	v_accvgpr_read_b32 v67, a99
	v_accvgpr_read_b32 v68, a100
	v_accvgpr_read_b32 v69, a101
	v_accvgpr_read_b32 v70, a102
	v_accvgpr_read_b32 v71, a103
	v_accvgpr_read_b32 v72, a104
	v_accvgpr_read_b32 v73, a105
	v_accvgpr_read_b32 v74, a106
	v_accvgpr_read_b32 v75, a107
	v_accvgpr_read_b32 v76, a108
	v_accvgpr_read_b32 v77, a109
	v_accvgpr_read_b32 v78, a110
	v_accvgpr_read_b32 v79, a111
	v_mul_f32_e32 v64, v64, v43
	v_mul_f32_e32 v65, v65, v43
	v_mul_f32_e32 v66, v66, v43
	v_mul_f32_e32 v67, v67, v43
	v_mul_f32_e32 v68, v68, v43
	v_mul_f32_e32 v69, v69, v43
	v_mul_f32_e32 v70, v70, v43
	v_mul_f32_e32 v71, v71, v43
	v_mul_f32_e32 v72, v72, v43
	v_mul_f32_e32 v73, v73, v43
	v_mul_f32_e32 v74, v74, v43
	v_mul_f32_e32 v75, v75, v43
	v_mul_f32_e32 v76, v76, v43
	v_mul_f32_e32 v77, v77, v43
	v_mul_f32_e32 v78, v78, v43
	v_mul_f32_e32 v79, v79, v43
	v_cvt_pk_f16_f32 v80, v64, v65
	v_cvt_pk_f16_f32 v81, v66, v67
	v_cvt_pk_f16_f32 v82, v68, v69
	v_cvt_pk_f16_f32 v83, v70, v71
	v_cvt_pk_f16_f32 v84, v72, v73
	v_cvt_pk_f16_f32 v85, v74, v75
	v_cvt_pk_f16_f32 v86, v76, v77
	v_cvt_pk_f16_f32 v87, v78, v79
	ds_write_b64 v112, v[80:81]
	ds_write_b64 v113, v[82:83]
	ds_write_b64 v114, v[84:85]
	ds_write_b64 v115, v[86:87]
	s_waitcnt lgkmcnt(0)
	ds_read_b128 v[136:139], v116
	ds_read_b128 v[140:143], v117
	ds_read_b128 v[144:147], v118
	ds_read_b128 v[148:151], v119
	ds_read_b128 v[152:155], v120
	ds_read_b128 v[156:159], v121
	ds_read_b128 v[160:163], v122
	ds_read_b128 v[164:167], v123
	s_waitcnt lgkmcnt(7)
	global_store_dwordx4 v[124:125], v[136:139], off sc1
	s_waitcnt lgkmcnt(6)
	global_store_dwordx4 v[124:125], v[140:143], off offset:1024 sc1
	s_waitcnt lgkmcnt(5)
	global_store_dwordx4 v[124:125], v[144:147], off offset:2048 sc1
	s_waitcnt lgkmcnt(4)
	global_store_dwordx4 v[124:125], v[148:151], off offset:3072 sc1
	s_waitcnt lgkmcnt(3)
	global_store_dwordx4 v[126:127], v[152:155], off sc1
	s_waitcnt lgkmcnt(2)
	global_store_dwordx4 v[126:127], v[156:159], off offset:1024 sc1
	s_waitcnt lgkmcnt(1)
	global_store_dwordx4 v[126:127], v[160:163], off offset:2048 sc1
	s_waitcnt lgkmcnt(0)
	global_store_dwordx4 v[126:127], v[164:167], off offset:3072 sc1
	v_rcp_f32_e32 v34, v132
	s_nop 1
	v_cmp_lt_f32_e32 vcc, 0, v132
	v_cndmask_b32_e32 v43, 0, v34, vcc
	s_waitcnt lgkmcnt(0)
	v_accvgpr_read_b32 v64, a16
	v_accvgpr_read_b32 v65, a17
	v_accvgpr_read_b32 v66, a18
	v_accvgpr_read_b32 v67, a19
	v_accvgpr_read_b32 v68, a20
	v_accvgpr_read_b32 v69, a21
	v_accvgpr_read_b32 v70, a22
	v_accvgpr_read_b32 v71, a23
	v_accvgpr_read_b32 v72, a24
	v_accvgpr_read_b32 v73, a25
	v_accvgpr_read_b32 v74, a26
	v_accvgpr_read_b32 v75, a27
	v_accvgpr_read_b32 v76, a28
	v_accvgpr_read_b32 v77, a29
	v_accvgpr_read_b32 v78, a30
	v_accvgpr_read_b32 v79, a31
	v_mul_f32_e32 v64, v64, v43
	v_mul_f32_e32 v65, v65, v43
	v_mul_f32_e32 v66, v66, v43
	v_mul_f32_e32 v67, v67, v43
	v_mul_f32_e32 v68, v68, v43
	v_mul_f32_e32 v69, v69, v43
	v_mul_f32_e32 v70, v70, v43
	v_mul_f32_e32 v71, v71, v43
	v_mul_f32_e32 v72, v72, v43
	v_mul_f32_e32 v73, v73, v43
	v_mul_f32_e32 v74, v74, v43
	v_mul_f32_e32 v75, v75, v43
	v_mul_f32_e32 v76, v76, v43
	v_mul_f32_e32 v77, v77, v43
	v_mul_f32_e32 v78, v78, v43
	v_mul_f32_e32 v79, v79, v43
	v_cvt_pk_f16_f32 v80, v64, v65
	v_cvt_pk_f16_f32 v81, v66, v67
	v_cvt_pk_f16_f32 v82, v68, v69
	v_cvt_pk_f16_f32 v83, v70, v71
	v_cvt_pk_f16_f32 v84, v72, v73
	v_cvt_pk_f16_f32 v85, v74, v75
	v_cvt_pk_f16_f32 v86, v76, v77
	v_cvt_pk_f16_f32 v87, v78, v79
	ds_write_b64 v100, v[80:81]
	ds_write_b64 v101, v[82:83]
	ds_write_b64 v102, v[84:85]
	ds_write_b64 v103, v[86:87]
	v_accvgpr_read_b32 v64, a48
	v_accvgpr_read_b32 v65, a49
	v_accvgpr_read_b32 v66, a50
	v_accvgpr_read_b32 v67, a51
	v_accvgpr_read_b32 v68, a52
	v_accvgpr_read_b32 v69, a53
	v_accvgpr_read_b32 v70, a54
	v_accvgpr_read_b32 v71, a55
	v_accvgpr_read_b32 v72, a56
	v_accvgpr_read_b32 v73, a57
	v_accvgpr_read_b32 v74, a58
	v_accvgpr_read_b32 v75, a59
	v_accvgpr_read_b32 v76, a60
	v_accvgpr_read_b32 v77, a61
	v_accvgpr_read_b32 v78, a62
	v_accvgpr_read_b32 v79, a63
	v_mul_f32_e32 v64, v64, v43
	v_mul_f32_e32 v65, v65, v43
	v_mul_f32_e32 v66, v66, v43
	v_mul_f32_e32 v67, v67, v43
	v_mul_f32_e32 v68, v68, v43
	v_mul_f32_e32 v69, v69, v43
	v_mul_f32_e32 v70, v70, v43
	v_mul_f32_e32 v71, v71, v43
	v_mul_f32_e32 v72, v72, v43
	v_mul_f32_e32 v73, v73, v43
	v_mul_f32_e32 v74, v74, v43
	v_mul_f32_e32 v75, v75, v43
	v_mul_f32_e32 v76, v76, v43
	v_mul_f32_e32 v77, v77, v43
	v_mul_f32_e32 v78, v78, v43
	v_mul_f32_e32 v79, v79, v43
	v_cvt_pk_f16_f32 v80, v64, v65
	v_cvt_pk_f16_f32 v81, v66, v67
	v_cvt_pk_f16_f32 v82, v68, v69
	v_cvt_pk_f16_f32 v83, v70, v71
	v_cvt_pk_f16_f32 v84, v72, v73
	v_cvt_pk_f16_f32 v85, v74, v75
	v_cvt_pk_f16_f32 v86, v76, v77
	v_cvt_pk_f16_f32 v87, v78, v79
	ds_write_b64 v104, v[80:81]
	ds_write_b64 v105, v[82:83]
	ds_write_b64 v106, v[84:85]
	ds_write_b64 v107, v[86:87]
	v_accvgpr_read_b32 v64, a80
	v_accvgpr_read_b32 v65, a81
	v_accvgpr_read_b32 v66, a82
	v_accvgpr_read_b32 v67, a83
	v_accvgpr_read_b32 v68, a84
	v_accvgpr_read_b32 v69, a85
	v_accvgpr_read_b32 v70, a86
	v_accvgpr_read_b32 v71, a87
	v_accvgpr_read_b32 v72, a88
	v_accvgpr_read_b32 v73, a89
	v_accvgpr_read_b32 v74, a90
	v_accvgpr_read_b32 v75, a91
	v_accvgpr_read_b32 v76, a92
	v_accvgpr_read_b32 v77, a93
	v_accvgpr_read_b32 v78, a94
	v_accvgpr_read_b32 v79, a95
	v_mul_f32_e32 v64, v64, v43
	v_mul_f32_e32 v65, v65, v43
	v_mul_f32_e32 v66, v66, v43
	v_mul_f32_e32 v67, v67, v43
	v_mul_f32_e32 v68, v68, v43
	v_mul_f32_e32 v69, v69, v43
	v_mul_f32_e32 v70, v70, v43
	v_mul_f32_e32 v71, v71, v43
	v_mul_f32_e32 v72, v72, v43
	v_mul_f32_e32 v73, v73, v43
	v_mul_f32_e32 v74, v74, v43
	v_mul_f32_e32 v75, v75, v43
	v_mul_f32_e32 v76, v76, v43
	v_mul_f32_e32 v77, v77, v43
	v_mul_f32_e32 v78, v78, v43
	v_mul_f32_e32 v79, v79, v43
	v_cvt_pk_f16_f32 v80, v64, v65
	v_cvt_pk_f16_f32 v81, v66, v67
	v_cvt_pk_f16_f32 v82, v68, v69
	v_cvt_pk_f16_f32 v83, v70, v71
	v_cvt_pk_f16_f32 v84, v72, v73
	v_cvt_pk_f16_f32 v85, v74, v75
	v_cvt_pk_f16_f32 v86, v76, v77
	v_cvt_pk_f16_f32 v87, v78, v79
	ds_write_b64 v108, v[80:81]
	ds_write_b64 v109, v[82:83]
	ds_write_b64 v110, v[84:85]
	ds_write_b64 v111, v[86:87]
	v_accvgpr_read_b32 v64, a112
	v_accvgpr_read_b32 v65, a113
	v_accvgpr_read_b32 v66, a114
	v_accvgpr_read_b32 v67, a115
	v_accvgpr_read_b32 v68, a116
	v_accvgpr_read_b32 v69, a117
	v_accvgpr_read_b32 v70, a118
	v_accvgpr_read_b32 v71, a119
	v_accvgpr_read_b32 v72, a120
	v_accvgpr_read_b32 v73, a121
	v_accvgpr_read_b32 v74, a122
	v_accvgpr_read_b32 v75, a123
	v_accvgpr_read_b32 v76, a124
	v_accvgpr_read_b32 v77, a125
	v_accvgpr_read_b32 v78, a126
	v_accvgpr_read_b32 v79, a127
	v_mul_f32_e32 v64, v64, v43
	v_mul_f32_e32 v65, v65, v43
	v_mul_f32_e32 v66, v66, v43
	v_mul_f32_e32 v67, v67, v43
	v_mul_f32_e32 v68, v68, v43
	v_mul_f32_e32 v69, v69, v43
	v_mul_f32_e32 v70, v70, v43
	v_mul_f32_e32 v71, v71, v43
	v_mul_f32_e32 v72, v72, v43
	v_mul_f32_e32 v73, v73, v43
	v_mul_f32_e32 v74, v74, v43
	v_mul_f32_e32 v75, v75, v43
	v_mul_f32_e32 v76, v76, v43
	v_mul_f32_e32 v77, v77, v43
	v_mul_f32_e32 v78, v78, v43
	v_mul_f32_e32 v79, v79, v43
	v_cvt_pk_f16_f32 v80, v64, v65
	v_cvt_pk_f16_f32 v81, v66, v67
	v_cvt_pk_f16_f32 v82, v68, v69
	v_cvt_pk_f16_f32 v83, v70, v71
	v_cvt_pk_f16_f32 v84, v72, v73
	v_cvt_pk_f16_f32 v85, v74, v75
	v_cvt_pk_f16_f32 v86, v76, v77
	v_cvt_pk_f16_f32 v87, v78, v79
	ds_write_b64 v112, v[80:81]
	ds_write_b64 v113, v[82:83]
	ds_write_b64 v114, v[84:85]
	ds_write_b64 v115, v[86:87]
	s_waitcnt lgkmcnt(0)
	ds_read_b128 v[136:139], v116
	ds_read_b128 v[140:143], v117
	ds_read_b128 v[144:147], v118
	ds_read_b128 v[148:151], v119
	ds_read_b128 v[152:155], v120
	ds_read_b128 v[156:159], v121
	ds_read_b128 v[160:163], v122
	ds_read_b128 v[164:167], v123
	s_waitcnt lgkmcnt(7)
	global_store_dwordx4 v[128:129], v[136:139], off sc1
	s_waitcnt lgkmcnt(6)
	global_store_dwordx4 v[128:129], v[140:143], off offset:1024 sc1
	s_waitcnt lgkmcnt(5)
	global_store_dwordx4 v[128:129], v[144:147], off offset:2048 sc1
	s_waitcnt lgkmcnt(4)
	global_store_dwordx4 v[128:129], v[148:151], off offset:3072 sc1
	s_waitcnt lgkmcnt(3)
	global_store_dwordx4 v[130:131], v[152:155], off sc1
	s_waitcnt lgkmcnt(2)
	global_store_dwordx4 v[130:131], v[156:159], off offset:1024 sc1
	s_waitcnt lgkmcnt(1)
	global_store_dwordx4 v[130:131], v[160:163], off offset:2048 sc1
	s_waitcnt lgkmcnt(0)
	global_store_dwordx4 v[130:131], v[164:167], off offset:3072 sc1
	s_waitcnt lgkmcnt(0)
	s_add_u32 s26, s26, s34
	s_addc_u32 s27, s27, 0
	v_cmp_gt_u64_e32 vcc, s[26:27], v[202:203]
	s_cbranch_vccnz .LBB2_64
	s_branch .LBB2_3
